# grid barriers before streaming phases (norm, quant, mixout, final) drop the cache invalidates; those phases read mutable rows with sc1 loads; on top of attention LDS-DMA
# speedup vs baseline: 1.0056x; 1.0056x over previous
.LBB0_446:
	s_or_b64 exec, exec, s[8:9]
	s_mov_b64 s[8:9], exec
	v_mbcnt_lo_u32_b32 v1, s8, 0
	v_mbcnt_hi_u32_b32 v1, s9, v1
	v_cmp_eq_u32_e32 vcc, 0, v1
	s_waitcnt vmcnt(0)
	s_and_saveexec_b64 s[10:11], vcc
	s_cbranch_execz .LBB0_448
	s_bcnt1_i32_b64 s2, s[8:9]
	v_mov_b32_e32 v1, 0x2000
	v_mov_b32_e32 v2, s2
	global_atomic_add v1, v2, s[6:7] offset:1024

.LBB0_464:
	v_lshlrev_b32_e32 v100, 2, v36
	v_mov_b32_e32 v101, v99
	v_lshl_add_u64 v[14:15], v[30:31], 0, v[100:101]
	global_load_dwordx4 v[2:5], v[14:15], off sc1
	s_and_b64 s[22:23], s[24:25], s[18:19]
	v_lshlrev_b64 v[96:97], 11, v[34:35]
	s_and_saveexec_b64 s[34:35], s[22:23]
	s_cbranch_execnz .LBB0_479
	s_or_b64 exec, exec, s[34:35]
	global_load_dwordx4 v[6:9], v[14:15], off offset:1024 sc1
	s_and_saveexec_b64 s[34:35], s[22:23]
	s_cbranch_execnz .LBB0_480
.LBB0_466:
	s_or_b64 exec, exec, s[34:35]
	global_load_dwordx4 v[10:13], v[14:15], off offset:2048 sc1
	s_and_saveexec_b64 s[34:35], s[22:23]
	s_cbranch_execnz .LBB0_481
.LBB0_467:
	s_or_b64 exec, exec, s[34:35]
	global_load_dwordx4 v[14:17], v[14:15], off offset:3072 sc1
	s_and_saveexec_b64 s[34:35], s[22:23]
	s_cbranch_execz .LBB0_469
.LBB0_468:
	v_lshl_add_u64 v[22:23], v[96:97], 2, v[88:89]
	global_load_dwordx4 v[18:21], v[22:23], off sc1
	s_waitcnt vmcnt(0)
	v_pk_add_f32 v[26:27], v[18:19], 0 op_sel_hi:[1,0]
	v_add_co_u32_e32 v18, vcc, 0x200000, v22
	v_pk_add_f32 v[24:25], v[20:21], 0 op_sel_hi:[1,0]
	s_nop 0
	v_addc_co_u32_e32 v19, vcc, 0, v23, vcc
	global_load_dwordx4 v[18:21], v[18:19], off sc1
	s_waitcnt vmcnt(0)
	v_pk_add_f32 v[26:27], v[26:27], v[18:19]
	v_add_co_u32_e32 v18, vcc, 0x400000, v22
	v_pk_add_f32 v[24:25], v[24:25], v[20:21]
	s_nop 0
	v_addc_co_u32_e32 v19, vcc, 0, v23, vcc
	global_load_dwordx4 v[18:21], v[18:19], off sc1
	s_waitcnt vmcnt(0)
	v_pk_add_f32 v[26:27], v[26:27], v[18:19]
	v_add_co_u32_e32 v18, vcc, 0x600000, v22
	v_pk_add_f32 v[24:25], v[24:25], v[20:21]
	s_nop 0
	v_addc_co_u32_e32 v19, vcc, 0, v23, vcc
	global_load_dwordx4 v[18:21], v[18:19], off sc1
	s_waitcnt vmcnt(0)
	v_pk_add_f32 v[26:27], v[26:27], v[18:19]
	v_add_co_u32_e32 v18, vcc, 0x800000, v22
	v_pk_add_f32 v[24:25], v[24:25], v[20:21]
	s_nop 0
	v_addc_co_u32_e32 v19, vcc, 0, v23, vcc
	global_load_dwordx4 v[18:21], v[18:19], off sc1
	s_waitcnt vmcnt(0)
	v_pk_add_f32 v[26:27], v[26:27], v[18:19]
	v_add_co_u32_e32 v18, vcc, 0xa00000, v22
	v_pk_add_f32 v[24:25], v[24:25], v[20:21]
	s_nop 0
	v_addc_co_u32_e32 v19, vcc, 0, v23, vcc
	global_load_dwordx4 v[18:21], v[18:19], off sc1
	s_waitcnt vmcnt(0)
	v_pk_add_f32 v[26:27], v[26:27], v[18:19]
	v_add_co_u32_e32 v18, vcc, 0xc00000, v22
	v_pk_add_f32 v[24:25], v[24:25], v[20:21]
	s_nop 0
	v_addc_co_u32_e32 v19, vcc, 0, v23, vcc
	global_load_dwordx4 v[18:21], v[18:19], off sc1
	s_waitcnt vmcnt(0)
	v_pk_add_f32 v[26:27], v[26:27], v[18:19]
	v_add_co_u32_e32 v18, vcc, 0xe00000, v22
	v_pk_add_f32 v[24:25], v[24:25], v[20:21]
	s_nop 0
	v_addc_co_u32_e32 v19, vcc, 0, v23, vcc
	global_load_dwordx4 v[18:21], v[18:19], off sc1
	s_waitcnt vmcnt(0)
	v_pk_add_f32 v[26:27], v[26:27], v[18:19]
	v_add_co_u32_e32 v18, vcc, 0x1000000, v22
	v_pk_add_f32 v[24:25], v[24:25], v[20:21]
	s_nop 0
	v_addc_co_u32_e32 v19, vcc, 0, v23, vcc
	global_load_dwordx4 v[18:21], v[18:19], off sc1
	s_waitcnt vmcnt(0)
	v_pk_add_f32 v[26:27], v[26:27], v[18:19]
	v_add_co_u32_e32 v18, vcc, 0x1200000, v22
	v_pk_add_f32 v[24:25], v[24:25], v[20:21]
	s_nop 0
	v_addc_co_u32_e32 v19, vcc, 0, v23, vcc
	global_load_dwordx4 v[18:21], v[18:19], off sc1
	s_waitcnt vmcnt(0)
	v_pk_add_f32 v[26:27], v[26:27], v[18:19]
	v_add_co_u32_e32 v18, vcc, 0x1400000, v22
	v_pk_add_f32 v[24:25], v[24:25], v[20:21]
	s_nop 0
	v_addc_co_u32_e32 v19, vcc, 0, v23, vcc
	global_load_dwordx4 v[18:21], v[18:19], off sc1
	s_waitcnt vmcnt(0)
	v_pk_add_f32 v[22:23], v[24:25], v[20:21]
	v_pk_add_f32 v[24:25], v[26:27], v[18:19]
	global_load_dwordx4 v[18:21], v[64:65], off sc1
	s_waitcnt vmcnt(0)
	v_pk_fma_f32 v[16:17], v[22:23], v[20:21], v[16:17]
	v_pk_fma_f32 v[14:15], v[24:25], v[18:19], v[14:15]
.LBB0_469:
	s_or_b64 exec, exec, s[34:35]
	v_lshlrev_b32_e32 v102, 2, v38
	v_mov_b32_e32 v103, v99
	v_lshl_add_u64 v[18:19], v[30:31], 0, v[102:103]
	global_load_dwordx4 v[18:21], v[18:19], off sc1
	s_and_saveexec_b64 s[34:35], s[22:23]
	s_cbranch_execz .LBB0_471
	v_lshl_add_u64 v[26:27], v[96:97], 2, v[66:67]
	global_load_dwordx4 v[22:25], v[26:27], off sc1
	s_waitcnt vmcnt(0)
	v_pk_add_f32 v[32:33], v[22:23], 0 op_sel_hi:[1,0]
	v_add_co_u32_e32 v22, vcc, 0x200000, v26
	v_pk_add_f32 v[28:29], v[24:25], 0 op_sel_hi:[1,0]
	s_nop 0
	v_addc_co_u32_e32 v23, vcc, 0, v27, vcc
	global_load_dwordx4 v[22:25], v[22:23], off sc1
	s_waitcnt vmcnt(0)
	v_pk_add_f32 v[32:33], v[32:33], v[22:23]
	v_add_co_u32_e32 v22, vcc, 0x400000, v26
	v_pk_add_f32 v[28:29], v[28:29], v[24:25]
	s_nop 0
	v_addc_co_u32_e32 v23, vcc, 0, v27, vcc
	global_load_dwordx4 v[22:25], v[22:23], off sc1
	s_waitcnt vmcnt(0)
	v_pk_add_f32 v[32:33], v[32:33], v[22:23]
	v_add_co_u32_e32 v22, vcc, 0x600000, v26
	v_pk_add_f32 v[28:29], v[28:29], v[24:25]
	s_nop 0
	v_addc_co_u32_e32 v23, vcc, 0, v27, vcc
	global_load_dwordx4 v[22:25], v[22:23], off sc1
	s_waitcnt vmcnt(0)
	v_pk_add_f32 v[32:33], v[32:33], v[22:23]
	v_add_co_u32_e32 v22, vcc, 0x800000, v26
	v_pk_add_f32 v[28:29], v[28:29], v[24:25]
	s_nop 0
	v_addc_co_u32_e32 v23, vcc, 0, v27, vcc
	global_load_dwordx4 v[22:25], v[22:23], off sc1
	s_waitcnt vmcnt(0)
	v_pk_add_f32 v[32:33], v[32:33], v[22:23]
	v_add_co_u32_e32 v22, vcc, 0xa00000, v26
	v_pk_add_f32 v[28:29], v[28:29], v[24:25]
	s_nop 0
	v_addc_co_u32_e32 v23, vcc, 0, v27, vcc
	global_load_dwordx4 v[22:25], v[22:23], off sc1
	s_waitcnt vmcnt(0)
	v_pk_add_f32 v[32:33], v[32:33], v[22:23]
	v_add_co_u32_e32 v22, vcc, 0xc00000, v26
	v_pk_add_f32 v[28:29], v[28:29], v[24:25]
	s_nop 0
	v_addc_co_u32_e32 v23, vcc, 0, v27, vcc
	global_load_dwordx4 v[22:25], v[22:23], off sc1
	s_waitcnt vmcnt(0)
	v_pk_add_f32 v[32:33], v[32:33], v[22:23]
	v_add_co_u32_e32 v22, vcc, 0xe00000, v26
	v_pk_add_f32 v[28:29], v[28:29], v[24:25]
	s_nop 0
	v_addc_co_u32_e32 v23, vcc, 0, v27, vcc
	global_load_dwordx4 v[22:25], v[22:23], off sc1
	s_waitcnt vmcnt(0)
	v_pk_add_f32 v[32:33], v[32:33], v[22:23]
	v_add_co_u32_e32 v22, vcc, 0x1000000, v26
	v_pk_add_f32 v[28:29], v[28:29], v[24:25]
	s_nop 0
	v_addc_co_u32_e32 v23, vcc, 0, v27, vcc
	global_load_dwordx4 v[22:25], v[22:23], off sc1
	s_waitcnt vmcnt(0)
	v_pk_add_f32 v[32:33], v[32:33], v[22:23]
	v_add_co_u32_e32 v22, vcc, 0x1200000, v26
	v_pk_add_f32 v[28:29], v[28:29], v[24:25]
	s_nop 0
	v_addc_co_u32_e32 v23, vcc, 0, v27, vcc
	global_load_dwordx4 v[22:25], v[22:23], off sc1
	s_waitcnt vmcnt(0)
	v_pk_add_f32 v[32:33], v[32:33], v[22:23]
	v_add_co_u32_e32 v22, vcc, 0x1400000, v26
	v_pk_add_f32 v[28:29], v[28:29], v[24:25]
	s_nop 0
	v_addc_co_u32_e32 v23, vcc, 0, v27, vcc
	global_load_dwordx4 v[22:25], v[22:23], off sc1
	s_waitcnt vmcnt(0)
	v_pk_add_f32 v[26:27], v[28:29], v[24:25]
	v_pk_add_f32 v[28:29], v[32:33], v[22:23]
	global_load_dwordx4 v[22:25], v[68:69], off sc1
	s_waitcnt vmcnt(0)
	v_pk_fma_f32 v[20:21], v[26:27], v[24:25], v[20:21]
	v_pk_fma_f32 v[18:19], v[28:29], v[22:23], v[18:19]
.LBB0_471:
	s_or_b64 exec, exec, s[34:35]
	v_lshlrev_b32_e32 v104, 2, v40
	v_mov_b32_e32 v105, v99
	v_lshl_add_u64 v[22:23], v[30:31], 0, v[104:105]
	global_load_dwordx4 v[22:25], v[22:23], off sc1
	s_and_saveexec_b64 s[34:35], s[22:23]
	s_cbranch_execz .LBB0_473
	v_lshl_add_u64 v[32:33], v[96:97], 2, v[70:71]
	global_load_dwordx4 v[26:29], v[32:33], off sc1
	s_waitcnt vmcnt(0)
	v_pk_add_f32 v[108:109], v[26:27], 0 op_sel_hi:[1,0]
	v_add_co_u32_e32 v26, vcc, 0x200000, v32
	v_pk_add_f32 v[106:107], v[28:29], 0 op_sel_hi:[1,0]
	s_nop 0
	v_addc_co_u32_e32 v27, vcc, 0, v33, vcc
	global_load_dwordx4 v[26:29], v[26:27], off sc1
	s_waitcnt vmcnt(0)
	v_pk_add_f32 v[108:109], v[108:109], v[26:27]
	v_add_co_u32_e32 v26, vcc, 0x400000, v32
	v_pk_add_f32 v[106:107], v[106:107], v[28:29]
	s_nop 0
	v_addc_co_u32_e32 v27, vcc, 0, v33, vcc
	global_load_dwordx4 v[26:29], v[26:27], off sc1
	s_waitcnt vmcnt(0)
	v_pk_add_f32 v[108:109], v[108:109], v[26:27]
	v_add_co_u32_e32 v26, vcc, 0x600000, v32
	v_pk_add_f32 v[106:107], v[106:107], v[28:29]
	s_nop 0
	v_addc_co_u32_e32 v27, vcc, 0, v33, vcc
	global_load_dwordx4 v[26:29], v[26:27], off sc1
	s_waitcnt vmcnt(0)
	v_pk_add_f32 v[108:109], v[108:109], v[26:27]
	v_add_co_u32_e32 v26, vcc, 0x800000, v32
	v_pk_add_f32 v[106:107], v[106:107], v[28:29]
	s_nop 0
	v_addc_co_u32_e32 v27, vcc, 0, v33, vcc
	global_load_dwordx4 v[26:29], v[26:27], off sc1
	s_waitcnt vmcnt(0)
	v_pk_add_f32 v[108:109], v[108:109], v[26:27]
	v_add_co_u32_e32 v26, vcc, 0xa00000, v32
	v_pk_add_f32 v[106:107], v[106:107], v[28:29]
	s_nop 0
	v_addc_co_u32_e32 v27, vcc, 0, v33, vcc
	global_load_dwordx4 v[26:29], v[26:27], off sc1
	s_waitcnt vmcnt(0)
	v_pk_add_f32 v[108:109], v[108:109], v[26:27]
	v_add_co_u32_e32 v26, vcc, 0xc00000, v32
	v_pk_add_f32 v[106:107], v[106:107], v[28:29]
	s_nop 0
	v_addc_co_u32_e32 v27, vcc, 0, v33, vcc
	global_load_dwordx4 v[26:29], v[26:27], off sc1
	s_waitcnt vmcnt(0)
	v_pk_add_f32 v[108:109], v[108:109], v[26:27]
	v_add_co_u32_e32 v26, vcc, 0xe00000, v32
	v_pk_add_f32 v[106:107], v[106:107], v[28:29]
	s_nop 0
	v_addc_co_u32_e32 v27, vcc, 0, v33, vcc
	global_load_dwordx4 v[26:29], v[26:27], off sc1
	s_waitcnt vmcnt(0)
	v_pk_add_f32 v[108:109], v[108:109], v[26:27]
	v_add_co_u32_e32 v26, vcc, 0x1000000, v32
	v_pk_add_f32 v[106:107], v[106:107], v[28:29]
	s_nop 0
	v_addc_co_u32_e32 v27, vcc, 0, v33, vcc
	global_load_dwordx4 v[26:29], v[26:27], off sc1
	s_waitcnt vmcnt(0)
	v_pk_add_f32 v[108:109], v[108:109], v[26:27]
	v_add_co_u32_e32 v26, vcc, 0x1200000, v32
	v_pk_add_f32 v[106:107], v[106:107], v[28:29]
	s_nop 0
	v_addc_co_u32_e32 v27, vcc, 0, v33, vcc
	global_load_dwordx4 v[26:29], v[26:27], off sc1
	s_waitcnt vmcnt(0)
	v_pk_add_f32 v[108:109], v[108:109], v[26:27]
	v_add_co_u32_e32 v26, vcc, 0x1400000, v32
	v_pk_add_f32 v[106:107], v[106:107], v[28:29]
	s_nop 0
	v_addc_co_u32_e32 v27, vcc, 0, v33, vcc
	global_load_dwordx4 v[26:29], v[26:27], off sc1
	s_waitcnt vmcnt(0)
	v_pk_add_f32 v[32:33], v[106:107], v[28:29]
	v_pk_add_f32 v[106:107], v[108:109], v[26:27]
	global_load_dwordx4 v[26:29], v[72:73], off sc1
	s_waitcnt vmcnt(0)
	v_pk_fma_f32 v[24:25], v[32:33], v[28:29], v[24:25]
	v_pk_fma_f32 v[22:23], v[106:107], v[26:27], v[22:23]
.LBB0_473:
	s_or_b64 exec, exec, s[34:35]
	v_lshlrev_b32_e32 v106, 2, v42
	v_mov_b32_e32 v107, v99
	v_lshl_add_u64 v[26:27], v[30:31], 0, v[106:107]
	global_load_dwordx4 v[26:29], v[26:27], off sc1
	s_and_saveexec_b64 s[34:35], s[22:23]
	s_cbranch_execz .LBB0_475
	v_lshl_add_u64 v[32:33], v[96:97], 2, v[74:75]
	global_load_dwordx4 v[108:111], v[32:33], off sc1
	s_waitcnt vmcnt(0)
	v_pk_add_f32 v[116:117], v[108:109], 0 op_sel_hi:[1,0]
	v_add_co_u32_e32 v108, vcc, 0x200000, v32
	v_pk_add_f32 v[112:113], v[110:111], 0 op_sel_hi:[1,0]
	s_nop 0
	v_addc_co_u32_e32 v109, vcc, 0, v33, vcc
	global_load_dwordx4 v[108:111], v[108:109], off sc1
	s_waitcnt vmcnt(0)
	v_pk_add_f32 v[116:117], v[116:117], v[108:109]
	v_add_co_u32_e32 v108, vcc, 0x400000, v32
	v_pk_add_f32 v[112:113], v[112:113], v[110:111]
	s_nop 0
	v_addc_co_u32_e32 v109, vcc, 0, v33, vcc
	global_load_dwordx4 v[108:111], v[108:109], off sc1
	s_waitcnt vmcnt(0)
	v_pk_add_f32 v[116:117], v[116:117], v[108:109]
	v_add_co_u32_e32 v108, vcc, 0x600000, v32
	v_pk_add_f32 v[112:113], v[112:113], v[110:111]
	s_nop 0
	v_addc_co_u32_e32 v109, vcc, 0, v33, vcc
	global_load_dwordx4 v[108:111], v[108:109], off sc1
	s_waitcnt vmcnt(0)
	v_pk_add_f32 v[116:117], v[116:117], v[108:109]
	v_add_co_u32_e32 v108, vcc, 0x800000, v32
	v_pk_add_f32 v[112:113], v[112:113], v[110:111]
	s_nop 0
	v_addc_co_u32_e32 v109, vcc, 0, v33, vcc
	global_load_dwordx4 v[108:111], v[108:109], off sc1
	s_waitcnt vmcnt(0)
	v_pk_add_f32 v[116:117], v[116:117], v[108:109]
	v_add_co_u32_e32 v108, vcc, 0xa00000, v32
	v_pk_add_f32 v[112:113], v[112:113], v[110:111]
	s_nop 0
	v_addc_co_u32_e32 v109, vcc, 0, v33, vcc
	global_load_dwordx4 v[108:111], v[108:109], off sc1
	s_waitcnt vmcnt(0)
	v_pk_add_f32 v[116:117], v[116:117], v[108:109]
	v_add_co_u32_e32 v108, vcc, 0xc00000, v32
	v_pk_add_f32 v[112:113], v[112:113], v[110:111]
	s_nop 0
	v_addc_co_u32_e32 v109, vcc, 0, v33, vcc
	global_load_dwordx4 v[108:111], v[108:109], off sc1
	s_waitcnt vmcnt(0)
	v_pk_add_f32 v[116:117], v[116:117], v[108:109]
	v_add_co_u32_e32 v108, vcc, 0xe00000, v32
	v_pk_add_f32 v[112:113], v[112:113], v[110:111]
	s_nop 0
	v_addc_co_u32_e32 v109, vcc, 0, v33, vcc
	global_load_dwordx4 v[108:111], v[108:109], off sc1
	s_waitcnt vmcnt(0)
	v_pk_add_f32 v[116:117], v[116:117], v[108:109]
	v_add_co_u32_e32 v108, vcc, 0x1000000, v32
	v_pk_add_f32 v[112:113], v[112:113], v[110:111]
	s_nop 0
	v_addc_co_u32_e32 v109, vcc, 0, v33, vcc
	global_load_dwordx4 v[108:111], v[108:109], off sc1
	s_waitcnt vmcnt(0)
	v_pk_add_f32 v[116:117], v[116:117], v[108:109]
	v_add_co_u32_e32 v108, vcc, 0x1200000, v32
	v_pk_add_f32 v[112:113], v[112:113], v[110:111]
	s_nop 0
	v_addc_co_u32_e32 v109, vcc, 0, v33, vcc
	global_load_dwordx4 v[108:111], v[108:109], off sc1
	v_add_co_u32_e32 v32, vcc, 0x1400000, v32
	s_waitcnt vmcnt(0)
	v_pk_add_f32 v[112:113], v[112:113], v[110:111]
	v_addc_co_u32_e32 v33, vcc, 0, v33, vcc
	v_pk_add_f32 v[116:117], v[116:117], v[108:109]
	global_load_dwordx4 v[108:111], v[32:33], off sc1
	s_waitcnt vmcnt(0)
	v_pk_add_f32 v[32:33], v[112:113], v[110:111]
	v_pk_add_f32 v[112:113], v[116:117], v[108:109]
	global_load_dwordx4 v[108:111], v[76:77], off sc1
	s_waitcnt vmcnt(0)
	v_pk_fma_f32 v[28:29], v[32:33], v[110:111], v[28:29]
	v_pk_fma_f32 v[26:27], v[112:113], v[108:109], v[26:27]
.LBB0_475:
	s_or_b64 exec, exec, s[34:35]
	v_lshlrev_b32_e32 v98, 2, v44
	v_lshl_add_u64 v[30:31], v[30:31], 0, v[98:99]
	global_load_dwordx4 v[30:33], v[30:31], off sc1
	s_and_saveexec_b64 s[34:35], s[22:23]
	s_cbranch_execz .LBB0_477
	v_lshl_add_u64 v[112:113], v[96:97], 2, v[78:79]
	global_load_dwordx4 v[108:111], v[112:113], off sc1
	s_waitcnt vmcnt(0)
	v_pk_add_f32 v[118:119], v[108:109], 0 op_sel_hi:[1,0]
	v_add_co_u32_e32 v108, vcc, 0x200000, v112
	v_pk_add_f32 v[116:117], v[110:111], 0 op_sel_hi:[1,0]
	s_nop 0
	v_addc_co_u32_e32 v109, vcc, 0, v113, vcc
	global_load_dwordx4 v[108:111], v[108:109], off sc1
	s_waitcnt vmcnt(0)
	v_pk_add_f32 v[118:119], v[118:119], v[108:109]
	v_add_co_u32_e32 v108, vcc, 0x400000, v112
	v_pk_add_f32 v[116:117], v[116:117], v[110:111]
	s_nop 0
	v_addc_co_u32_e32 v109, vcc, 0, v113, vcc
	global_load_dwordx4 v[108:111], v[108:109], off sc1
	s_waitcnt vmcnt(0)
	v_pk_add_f32 v[118:119], v[118:119], v[108:109]
	v_add_co_u32_e32 v108, vcc, 0x600000, v112
	v_pk_add_f32 v[116:117], v[116:117], v[110:111]
	s_nop 0
	v_addc_co_u32_e32 v109, vcc, 0, v113, vcc
	global_load_dwordx4 v[108:111], v[108:109], off sc1
	s_waitcnt vmcnt(0)
	v_pk_add_f32 v[118:119], v[118:119], v[108:109]
	v_add_co_u32_e32 v108, vcc, 0x800000, v112
	v_pk_add_f32 v[116:117], v[116:117], v[110:111]
	s_nop 0
	v_addc_co_u32_e32 v109, vcc, 0, v113, vcc
	global_load_dwordx4 v[108:111], v[108:109], off sc1
	s_waitcnt vmcnt(0)
	v_pk_add_f32 v[118:119], v[118:119], v[108:109]
	v_add_co_u32_e32 v108, vcc, 0xa00000, v112
	v_pk_add_f32 v[116:117], v[116:117], v[110:111]
	s_nop 0
	v_addc_co_u32_e32 v109, vcc, 0, v113, vcc
	global_load_dwordx4 v[108:111], v[108:109], off sc1
	s_waitcnt vmcnt(0)
	v_pk_add_f32 v[118:119], v[118:119], v[108:109]
	v_add_co_u32_e32 v108, vcc, 0xc00000, v112
	v_pk_add_f32 v[116:117], v[116:117], v[110:111]
	s_nop 0
	v_addc_co_u32_e32 v109, vcc, 0, v113, vcc
	global_load_dwordx4 v[108:111], v[108:109], off sc1
	s_waitcnt vmcnt(0)
	v_pk_add_f32 v[118:119], v[118:119], v[108:109]
	v_add_co_u32_e32 v108, vcc, 0xe00000, v112
	v_pk_add_f32 v[116:117], v[116:117], v[110:111]
	s_nop 0
	v_addc_co_u32_e32 v109, vcc, 0, v113, vcc
	global_load_dwordx4 v[108:111], v[108:109], off sc1
	s_waitcnt vmcnt(0)
	v_pk_add_f32 v[118:119], v[118:119], v[108:109]
	v_add_co_u32_e32 v108, vcc, 0x1000000, v112
	v_pk_add_f32 v[116:117], v[116:117], v[110:111]
	s_nop 0
	v_addc_co_u32_e32 v109, vcc, 0, v113, vcc
	global_load_dwordx4 v[108:111], v[108:109], off sc1
	s_waitcnt vmcnt(0)
	v_pk_add_f32 v[118:119], v[118:119], v[108:109]
	v_add_co_u32_e32 v108, vcc, 0x1200000, v112
	v_pk_add_f32 v[116:117], v[116:117], v[110:111]
	s_nop 0
	v_addc_co_u32_e32 v109, vcc, 0, v113, vcc
	global_load_dwordx4 v[108:111], v[108:109], off sc1
	s_waitcnt vmcnt(0)
	v_pk_add_f32 v[118:119], v[118:119], v[108:109]
	v_add_co_u32_e32 v108, vcc, 0x1400000, v112
	v_pk_add_f32 v[116:117], v[116:117], v[110:111]
	s_nop 0
	v_addc_co_u32_e32 v109, vcc, 0, v113, vcc
	global_load_dwordx4 v[108:111], v[108:109], off sc1
	s_waitcnt vmcnt(0)
	v_pk_add_f32 v[112:113], v[116:117], v[110:111]
	v_pk_add_f32 v[116:117], v[118:119], v[108:109]
	global_load_dwordx4 v[108:111], v[80:81], off sc1
	s_waitcnt vmcnt(0)
	v_pk_fma_f32 v[32:33], v[112:113], v[110:111], v[32:33]
	v_pk_fma_f32 v[30:31], v[116:117], v[108:109], v[30:31]

.LBB0_479:
	v_lshl_add_u64 v[10:11], v[96:97], 2, v[56:57]
	global_load_dwordx4 v[6:9], v[10:11], off sc1
	s_waitcnt vmcnt(0)
	v_pk_add_f32 v[16:17], v[6:7], 0 op_sel_hi:[1,0]
	v_add_co_u32_e32 v6, vcc, 0x200000, v10
	v_pk_add_f32 v[12:13], v[8:9], 0 op_sel_hi:[1,0]
	s_nop 0
	v_addc_co_u32_e32 v7, vcc, 0, v11, vcc
	global_load_dwordx4 v[6:9], v[6:7], off sc1
	s_waitcnt vmcnt(0)
	v_pk_add_f32 v[16:17], v[16:17], v[6:7]
	v_add_co_u32_e32 v6, vcc, 0x400000, v10
	v_pk_add_f32 v[12:13], v[12:13], v[8:9]
	s_nop 0
	v_addc_co_u32_e32 v7, vcc, 0, v11, vcc
	global_load_dwordx4 v[6:9], v[6:7], off sc1
	s_waitcnt vmcnt(0)
	v_pk_add_f32 v[16:17], v[16:17], v[6:7]
	v_add_co_u32_e32 v6, vcc, 0x600000, v10
	v_pk_add_f32 v[12:13], v[12:13], v[8:9]
	s_nop 0
	v_addc_co_u32_e32 v7, vcc, 0, v11, vcc
	global_load_dwordx4 v[6:9], v[6:7], off sc1
	s_waitcnt vmcnt(0)
	v_pk_add_f32 v[16:17], v[16:17], v[6:7]
	v_add_co_u32_e32 v6, vcc, 0x800000, v10
	v_pk_add_f32 v[12:13], v[12:13], v[8:9]
	s_nop 0
	v_addc_co_u32_e32 v7, vcc, 0, v11, vcc
	global_load_dwordx4 v[6:9], v[6:7], off sc1
	s_waitcnt vmcnt(0)
	v_pk_add_f32 v[16:17], v[16:17], v[6:7]
	v_add_co_u32_e32 v6, vcc, 0xa00000, v10
	v_pk_add_f32 v[12:13], v[12:13], v[8:9]
	s_nop 0
	v_addc_co_u32_e32 v7, vcc, 0, v11, vcc
	global_load_dwordx4 v[6:9], v[6:7], off sc1
	s_waitcnt vmcnt(0)
	v_pk_add_f32 v[16:17], v[16:17], v[6:7]
	v_add_co_u32_e32 v6, vcc, 0xc00000, v10
	v_pk_add_f32 v[12:13], v[12:13], v[8:9]
	s_nop 0
	v_addc_co_u32_e32 v7, vcc, 0, v11, vcc
	global_load_dwordx4 v[6:9], v[6:7], off sc1
	s_waitcnt vmcnt(0)
	v_pk_add_f32 v[16:17], v[16:17], v[6:7]
	v_add_co_u32_e32 v6, vcc, 0xe00000, v10
	v_pk_add_f32 v[12:13], v[12:13], v[8:9]
	s_nop 0
	v_addc_co_u32_e32 v7, vcc, 0, v11, vcc
	global_load_dwordx4 v[6:9], v[6:7], off sc1
	s_waitcnt vmcnt(0)
	v_pk_add_f32 v[16:17], v[16:17], v[6:7]
	v_add_co_u32_e32 v6, vcc, 0x1000000, v10
	v_pk_add_f32 v[12:13], v[12:13], v[8:9]
	s_nop 0
	v_addc_co_u32_e32 v7, vcc, 0, v11, vcc
	global_load_dwordx4 v[6:9], v[6:7], off sc1
	s_waitcnt vmcnt(0)
	v_pk_add_f32 v[16:17], v[16:17], v[6:7]
	v_add_co_u32_e32 v6, vcc, 0x1200000, v10
	v_pk_add_f32 v[12:13], v[12:13], v[8:9]
	s_nop 0
	v_addc_co_u32_e32 v7, vcc, 0, v11, vcc
	global_load_dwordx4 v[6:9], v[6:7], off sc1
	s_waitcnt vmcnt(0)
	v_pk_add_f32 v[16:17], v[16:17], v[6:7]
	v_add_co_u32_e32 v6, vcc, 0x1400000, v10
	v_pk_add_f32 v[12:13], v[12:13], v[8:9]
	s_nop 0
	v_addc_co_u32_e32 v7, vcc, 0, v11, vcc
	global_load_dwordx4 v[6:9], v[6:7], off sc1
	s_waitcnt vmcnt(0)
	v_pk_add_f32 v[10:11], v[12:13], v[8:9]
	v_pk_add_f32 v[12:13], v[16:17], v[6:7]
	global_load_dwordx4 v[6:9], v[58:59], off sc1
	s_waitcnt vmcnt(0)
	v_pk_fma_f32 v[4:5], v[10:11], v[8:9], v[4:5]
	v_pk_fma_f32 v[2:3], v[12:13], v[6:7], v[2:3]
	s_or_b64 exec, exec, s[34:35]
	global_load_dwordx4 v[6:9], v[14:15], off offset:1024 sc1
	s_and_saveexec_b64 s[34:35], s[22:23]
	s_cbranch_execz .LBB0_466
.LBB0_480:
	v_lshl_add_u64 v[16:17], v[96:97], 2, v[84:85]
	global_load_dwordx4 v[10:13], v[16:17], off sc1
	s_waitcnt vmcnt(0)
	v_pk_add_f32 v[20:21], v[10:11], 0 op_sel_hi:[1,0]
	v_add_co_u32_e32 v10, vcc, 0x200000, v16
	v_pk_add_f32 v[18:19], v[12:13], 0 op_sel_hi:[1,0]
	s_nop 0
	v_addc_co_u32_e32 v11, vcc, 0, v17, vcc
	global_load_dwordx4 v[10:13], v[10:11], off sc1
	s_waitcnt vmcnt(0)
	v_pk_add_f32 v[20:21], v[20:21], v[10:11]
	v_add_co_u32_e32 v10, vcc, 0x400000, v16
	v_pk_add_f32 v[18:19], v[18:19], v[12:13]
	s_nop 0
	v_addc_co_u32_e32 v11, vcc, 0, v17, vcc
	global_load_dwordx4 v[10:13], v[10:11], off sc1
	s_waitcnt vmcnt(0)
	v_pk_add_f32 v[20:21], v[20:21], v[10:11]
	v_add_co_u32_e32 v10, vcc, 0x600000, v16
	v_pk_add_f32 v[18:19], v[18:19], v[12:13]
	s_nop 0
	v_addc_co_u32_e32 v11, vcc, 0, v17, vcc
	global_load_dwordx4 v[10:13], v[10:11], off sc1
	s_waitcnt vmcnt(0)
	v_pk_add_f32 v[20:21], v[20:21], v[10:11]
	v_add_co_u32_e32 v10, vcc, 0x800000, v16
	v_pk_add_f32 v[18:19], v[18:19], v[12:13]
	s_nop 0
	v_addc_co_u32_e32 v11, vcc, 0, v17, vcc
	global_load_dwordx4 v[10:13], v[10:11], off sc1
	s_waitcnt vmcnt(0)
	v_pk_add_f32 v[20:21], v[20:21], v[10:11]
	v_add_co_u32_e32 v10, vcc, 0xa00000, v16
	v_pk_add_f32 v[18:19], v[18:19], v[12:13]
	s_nop 0
	v_addc_co_u32_e32 v11, vcc, 0, v17, vcc
	global_load_dwordx4 v[10:13], v[10:11], off sc1
	s_waitcnt vmcnt(0)
	v_pk_add_f32 v[20:21], v[20:21], v[10:11]
	v_add_co_u32_e32 v10, vcc, 0xc00000, v16
	v_pk_add_f32 v[18:19], v[18:19], v[12:13]
	s_nop 0
	v_addc_co_u32_e32 v11, vcc, 0, v17, vcc
	global_load_dwordx4 v[10:13], v[10:11], off sc1
	s_waitcnt vmcnt(0)
	v_pk_add_f32 v[20:21], v[20:21], v[10:11]
	v_add_co_u32_e32 v10, vcc, 0xe00000, v16
	v_pk_add_f32 v[18:19], v[18:19], v[12:13]
	s_nop 0
	v_addc_co_u32_e32 v11, vcc, 0, v17, vcc
	global_load_dwordx4 v[10:13], v[10:11], off sc1
	s_waitcnt vmcnt(0)
	v_pk_add_f32 v[20:21], v[20:21], v[10:11]
	v_add_co_u32_e32 v10, vcc, 0x1000000, v16
	v_pk_add_f32 v[18:19], v[18:19], v[12:13]
	s_nop 0
	v_addc_co_u32_e32 v11, vcc, 0, v17, vcc
	global_load_dwordx4 v[10:13], v[10:11], off sc1
	s_waitcnt vmcnt(0)
	v_pk_add_f32 v[20:21], v[20:21], v[10:11]
	v_add_co_u32_e32 v10, vcc, 0x1200000, v16
	v_pk_add_f32 v[18:19], v[18:19], v[12:13]
	s_nop 0
	v_addc_co_u32_e32 v11, vcc, 0, v17, vcc
	global_load_dwordx4 v[10:13], v[10:11], off sc1
	s_waitcnt vmcnt(0)
	v_pk_add_f32 v[20:21], v[20:21], v[10:11]
	v_add_co_u32_e32 v10, vcc, 0x1400000, v16
	v_pk_add_f32 v[18:19], v[18:19], v[12:13]
	s_nop 0
	v_addc_co_u32_e32 v11, vcc, 0, v17, vcc
	global_load_dwordx4 v[10:13], v[10:11], off sc1
	s_waitcnt vmcnt(0)
	v_pk_add_f32 v[16:17], v[18:19], v[12:13]
	v_pk_add_f32 v[18:19], v[20:21], v[10:11]
	global_load_dwordx4 v[10:13], v[60:61], off sc1
	s_waitcnt vmcnt(0)
	v_pk_fma_f32 v[8:9], v[16:17], v[12:13], v[8:9]
	v_pk_fma_f32 v[6:7], v[18:19], v[10:11], v[6:7]
	s_or_b64 exec, exec, s[34:35]
	global_load_dwordx4 v[10:13], v[14:15], off offset:2048 sc1
	s_and_saveexec_b64 s[34:35], s[22:23]
	s_cbranch_execz .LBB0_467
.LBB0_481:
	v_lshl_add_u64 v[20:21], v[96:97], 2, v[86:87]
	global_load_dwordx4 v[16:19], v[20:21], off sc1
	s_waitcnt vmcnt(0)
	v_pk_add_f32 v[24:25], v[16:17], 0 op_sel_hi:[1,0]
	v_add_co_u32_e32 v16, vcc, 0x200000, v20
	v_pk_add_f32 v[22:23], v[18:19], 0 op_sel_hi:[1,0]
	s_nop 0
	v_addc_co_u32_e32 v17, vcc, 0, v21, vcc
	global_load_dwordx4 v[16:19], v[16:17], off sc1
	s_waitcnt vmcnt(0)
	v_pk_add_f32 v[24:25], v[24:25], v[16:17]
	v_add_co_u32_e32 v16, vcc, 0x400000, v20
	v_pk_add_f32 v[22:23], v[22:23], v[18:19]
	s_nop 0
	v_addc_co_u32_e32 v17, vcc, 0, v21, vcc
	global_load_dwordx4 v[16:19], v[16:17], off sc1
	s_waitcnt vmcnt(0)
	v_pk_add_f32 v[24:25], v[24:25], v[16:17]
	v_add_co_u32_e32 v16, vcc, 0x600000, v20
	v_pk_add_f32 v[22:23], v[22:23], v[18:19]
	s_nop 0
	v_addc_co_u32_e32 v17, vcc, 0, v21, vcc
	global_load_dwordx4 v[16:19], v[16:17], off sc1
	s_waitcnt vmcnt(0)
	v_pk_add_f32 v[24:25], v[24:25], v[16:17]
	v_add_co_u32_e32 v16, vcc, 0x800000, v20
	v_pk_add_f32 v[22:23], v[22:23], v[18:19]
	s_nop 0
	v_addc_co_u32_e32 v17, vcc, 0, v21, vcc
	global_load_dwordx4 v[16:19], v[16:17], off sc1
	s_waitcnt vmcnt(0)
	v_pk_add_f32 v[24:25], v[24:25], v[16:17]
	v_add_co_u32_e32 v16, vcc, 0xa00000, v20
	v_pk_add_f32 v[22:23], v[22:23], v[18:19]
	s_nop 0
	v_addc_co_u32_e32 v17, vcc, 0, v21, vcc
	global_load_dwordx4 v[16:19], v[16:17], off sc1
	s_waitcnt vmcnt(0)
	v_pk_add_f32 v[24:25], v[24:25], v[16:17]
	v_add_co_u32_e32 v16, vcc, 0xc00000, v20
	v_pk_add_f32 v[22:23], v[22:23], v[18:19]
	s_nop 0
	v_addc_co_u32_e32 v17, vcc, 0, v21, vcc
	global_load_dwordx4 v[16:19], v[16:17], off sc1
	s_waitcnt vmcnt(0)
	v_pk_add_f32 v[24:25], v[24:25], v[16:17]
	v_add_co_u32_e32 v16, vcc, 0xe00000, v20
	v_pk_add_f32 v[22:23], v[22:23], v[18:19]
	s_nop 0
	v_addc_co_u32_e32 v17, vcc, 0, v21, vcc
	global_load_dwordx4 v[16:19], v[16:17], off sc1
	s_waitcnt vmcnt(0)
	v_pk_add_f32 v[24:25], v[24:25], v[16:17]
	v_add_co_u32_e32 v16, vcc, 0x1000000, v20
	v_pk_add_f32 v[22:23], v[22:23], v[18:19]
	s_nop 0
	v_addc_co_u32_e32 v17, vcc, 0, v21, vcc
	global_load_dwordx4 v[16:19], v[16:17], off sc1
	s_waitcnt vmcnt(0)
	v_pk_add_f32 v[24:25], v[24:25], v[16:17]
	v_add_co_u32_e32 v16, vcc, 0x1200000, v20
	v_pk_add_f32 v[22:23], v[22:23], v[18:19]
	s_nop 0
	v_addc_co_u32_e32 v17, vcc, 0, v21, vcc
	global_load_dwordx4 v[16:19], v[16:17], off sc1
	s_waitcnt vmcnt(0)
	v_pk_add_f32 v[24:25], v[24:25], v[16:17]
	v_add_co_u32_e32 v16, vcc, 0x1400000, v20
	v_pk_add_f32 v[22:23], v[22:23], v[18:19]
	s_nop 0
	v_addc_co_u32_e32 v17, vcc, 0, v21, vcc
	global_load_dwordx4 v[16:19], v[16:17], off sc1
	s_waitcnt vmcnt(0)
	v_pk_add_f32 v[20:21], v[22:23], v[18:19]
	v_pk_add_f32 v[22:23], v[24:25], v[16:17]
	global_load_dwordx4 v[16:19], v[62:63], off sc1
	s_waitcnt vmcnt(0)
	v_pk_fma_f32 v[12:13], v[20:21], v[18:19], v[12:13]
	v_pk_fma_f32 v[10:11], v[22:23], v[16:17], v[10:11]
	s_or_b64 exec, exec, s[34:35]
	global_load_dwordx4 v[14:17], v[14:15], off offset:3072 sc1
	s_and_saveexec_b64 s[34:35], s[22:23]
	s_cbranch_execnz .LBB0_468
	s_branch .LBB0_469

.LBB0_1518:
	s_or_b64 exec, exec, s[4:5]
	s_mov_b64 s[22:23], exec
	v_mbcnt_lo_u32_b32 v1, s22, 0
	v_mbcnt_hi_u32_b32 v1, s23, v1
	v_cmp_eq_u32_e32 vcc, 0, v1
	s_waitcnt vmcnt(0)
	s_and_saveexec_b64 s[24:25], vcc
	s_cbranch_execz .LBB0_1520
	s_bcnt1_i32_b64 s3, s[22:23]
	v_mov_b32_e32 v1, s3
	v_mov_b32_e32 v2, 0x2000
	global_atomic_add v2, v1, s[18:19] offset:1024

.LBB0_1524:
	v_ashrrev_i32_e32 v67, 31, v66
	v_lshlrev_b64 v[2:3], 11, v[66:67]
	v_lshl_add_u64 v[2:3], v[72:73], 0, v[2:3]
	s_movk_i32 s3, 0x3200
	v_add_co_u32_e32 v14, vcc, 0x3d5fd000, v2
	v_mad_i64_i32 v[4:5], s[4:5], v66, s3, v[74:75]
	s_nop 0
	v_addc_co_u32_e32 v15, vcc, 0, v3, vcc
	s_mov_b64 s[4:5], 0x3d5fd600
	v_add_co_u32_e32 v16, vcc, 0x3f67d000, v2
	v_lshl_add_u64 v[6:7], v[2:3], 0, s[4:5]
	s_mov_b64 s[4:5], 0x3f67d600
	v_addc_co_u32_e32 v17, vcc, 0, v3, vcc
	v_lshl_add_u64 v[8:9], v[2:3], 0, s[4:5]
	s_mov_b64 s[4:5], 0x416fd600
	v_add_co_u32_e32 v18, vcc, 0x416fd000, v2
	global_load_dwordx4 v[10:13], v[68:69], off offset:16 sc1
	global_load_dwordx4 v[26:29], v[68:69], off sc1
	global_load_dwordx4 v[42:45], v[14:15], off offset:1536 sc1
	global_load_dwordx4 v[34:37], v[8:9], off offset:16 sc1
	global_load_dwordx4 v[38:41], v[6:7], off offset:16 sc1
	global_load_dwordx4 v[30:33], v[4:5], off offset:3072 sc1
	v_lshl_add_u64 v[6:7], v[2:3], 0, s[4:5]
	s_mov_b64 s[4:5], 0x4377d600
	v_addc_co_u32_e32 v19, vcc, 0, v3, vcc
	v_lshl_add_u64 v[14:15], v[2:3], 0, s[4:5]
	v_add_co_u32_e32 v2, vcc, 0x4377d000, v2
	global_load_dwordx4 v[46:49], v[16:17], off offset:1536 sc1
	s_nop 0
	global_load_dwordx4 v[6:9], v[6:7], off offset:16 sc1
	v_addc_co_u32_e32 v3, vcc, 0, v3, vcc
	v_add_co_u32_e32 v4, vcc, 0x2000, v4
	global_load_dwordx4 v[18:21], v[18:19], off offset:1536 sc1
	s_nop 0
	global_load_dwordx4 v[14:17], v[14:15], off offset:16 sc1
	v_addc_co_u32_e32 v5, vcc, 0, v5, vcc
	global_load_dwordx4 v[22:25], v[2:3], off offset:1536 sc1
	s_nop 0
	global_load_dwordx4 v[2:5], v[4:5], off offset:2048 sc1
	v_add_u32_e32 v50, 0xffffff00, v66
	s_movk_i32 s3, 0x400
	v_cmp_gt_u32_e32 vcc, s3, v50
	s_and_saveexec_b64 s[22:23], vcc
	s_cbranch_execz .LBB0_1523
	v_lshrrev_b32_e32 v51, 6, v50
	v_and_b32_e32 v51, 8, v51
	v_bfe_u32 v50, v50, 8, 1
	v_or3_b32 v50, v51, v1, v50
	v_readlane_b32 s4, v253, 24
	v_mul_u32_u24_e32 v50, 0x82000, v50
	v_mov_b32_e32 v51, v99
	v_readlane_b32 s5, v253, 25
	v_mov_b32_e32 v52, 3
	v_lshlrev_b32_sdwa v52, v52, v66 dst_sel:DWORD dst_unused:UNUSED_PAD src0_sel:DWORD src1_sel:BYTE_0
	v_lshl_add_u64 v[50:51], s[4:5], 0, v[50:51]
	v_mov_b32_e32 v53, v99
	v_lshl_add_u64 v[52:53], v[50:51], 0, v[52:53]
	v_add_co_u32_e32 v54, vcc, 0x20000, v52
	s_mov_b32 s3, 0xff61b1e6
	s_nop 0
	v_addc_co_u32_e32 v55, vcc, 0, v53, vcc
	global_load_dwordx2 v[60:61], v[54:55], off sc1
	v_add_co_u32_e32 v54, vcc, 0x40000, v52
	s_mov_b64 s[4:5], 0x20800
	s_nop 0
	v_addc_co_u32_e32 v55, vcc, 0, v53, vcc
	global_load_dwordx2 v[62:63], v[54:55], off offset:2048 sc1
	v_add_co_u32_e32 v54, vcc, 0x61000, v52
	s_waitcnt vmcnt(0)
	v_max3_f32 v56, v60, s3, v62
	v_addc_co_u32_e32 v55, vcc, 0, v53, vcc
	v_add_co_u32_e32 v52, vcc, 0x81000, v52
	global_load_dwordx2 v[64:65], v[54:55], off sc1
	s_nop 0
	v_addc_co_u32_e32 v53, vcc, 0, v53, vcc
	global_load_dwordx2 v[92:93], v[52:53], off offset:2048 sc1
	v_mov_b32_e32 v52, 9
	v_lshlrev_b32_sdwa v52, v52, v66 dst_sel:DWORD dst_unused:UNUSED_PAD src0_sel:DWORD src1_sel:BYTE_0
	v_mov_b32_e32 v53, v99
	v_lshl_add_u64 v[50:51], v[50:51], 0, v[52:53]
	v_lshlrev_b32_e32 v52, 2, v70
	v_lshl_add_u64 v[58:59], v[50:51], 0, v[52:53]
	s_mov_b32 s3, 0x20000
	v_lshl_add_u64 v[82:83], v[58:59], 0, s[4:5]
	s_mov_b64 s[4:5], 0x41000
	s_waitcnt vmcnt(0)
	v_max3_f32 v91, v56, v64, v92
	v_sub_f32_e32 v50, v60, v91
	v_sub_f32_e32 v60, v62, v91
	v_mul_f32_e32 v50, 0x3dd53b94, v50
	v_mul_f32_e32 v60, 0x3dd53b94, v60
	v_exp_f32_e32 v87, v50
	v_exp_f32_e32 v86, v60
	v_mov_b32_e32 v60, v63
	global_load_dwordx4 v[50:53], v[58:59], off offset:16 sc1
	global_load_dwordx4 v[54:57], v[58:59], off sc1
	v_mov_b32_e32 v96, v87
	v_pk_mul_f32 v[94:95], v[60:61], v[86:87]
	v_add_co_u32_e32 v60, vcc, s3, v58
	v_mov_b32_e32 v97, v86
	s_nop 0
	v_addc_co_u32_e32 v61, vcc, 0, v59, vcc
	global_load_dwordx4 v[60:63], v[60:61], off offset:2048 sc1
	s_nop 0
	global_load_dwordx4 v[82:85], v[82:83], off offset:16 sc1
	s_mov_b32 s3, 0x41000
	v_add_f32_e32 v95, 0, v95
	s_waitcnt vmcnt(2)
	v_mov_b32_e32 v88, v54
	s_waitcnt vmcnt(1)
	v_mov_b32_e32 v89, v60
	v_pk_mul_f32 v[86:87], v[88:89], v[96:97]
	v_mov_b32_e32 v60, v55
	v_add_f32_e32 v54, 0, v86
	v_add_f32_e32 v90, v54, v87
	v_mov_b32_e32 v86, v50
	s_waitcnt vmcnt(0)
	v_mov_b32_e32 v87, v82
	v_pk_mul_f32 v[86:87], v[96:97], v[86:87]
	v_pk_mul_f32 v[54:55], v[60:61], v[96:97]
	v_add_f32_e32 v50, 0, v86
	v_add_f32_e32 v89, v50, v87
	v_add_f32_e32 v50, 0, v54
	v_mov_b32_e32 v82, v51
	v_add_f32_e32 v88, v50, v55
	v_pk_mul_f32 v[50:51], v[96:97], v[82:83]
	v_sub_f32_e32 v61, v92, v91
	v_add_f32_e32 v50, 0, v50
	v_add_f32_e32 v87, v50, v51
	v_mov_b32_e32 v50, v56
	v_mov_b32_e32 v51, v62
	v_pk_mul_f32 v[50:51], v[50:51], v[96:97]
	v_mov_b32_e32 v62, v57
	v_add_f32_e32 v50, 0, v50
	v_add_f32_e32 v86, v50, v51
	v_mov_b32_e32 v50, v52
	v_mov_b32_e32 v51, v84
	v_pk_mul_f32 v[50:51], v[96:97], v[50:51]
	v_mov_b32_e32 v84, v53
	v_add_f32_e32 v50, 0, v50
	v_add_f32_e32 v81, v50, v51
	v_pk_mul_f32 v[50:51], v[62:63], v[96:97]
	v_mul_f32_e32 v61, 0x3dd53b94, v61
	v_add_f32_e32 v50, 0, v50
	v_add_f32_e32 v79, v50, v51
	v_pk_mul_f32 v[50:51], v[96:97], v[84:85]
	v_exp_f32_e32 v84, v61
	v_add_f32_e32 v50, 0, v50
	v_add_f32_e32 v71, v50, v51
	v_sub_f32_e32 v50, v64, v91
	v_mul_f32_e32 v50, 0x3dd53b94, v50
	v_exp_f32_e32 v85, v50
	v_add_co_u32_e32 v52, vcc, s3, v58
	v_lshl_add_u64 v[50:51], v[58:59], 0, s[4:5]
	s_nop 0
	v_addc_co_u32_e32 v53, vcc, 0, v59, vcc
	s_mov_b64 s[4:5], 0x61800
	s_mov_b32 s3, 0x61000
	v_mov_b32_e32 v64, v93
	v_lshl_add_u64 v[62:63], v[58:59], 0, s[4:5]
	v_add_co_u32_e32 v58, vcc, s3, v58
	v_add_f32_e32 v60, v94, v95
	v_pk_mul_f32 v[82:83], v[64:65], v[84:85]
	v_addc_co_u32_e32 v59, vcc, 0, v59, vcc
	global_load_dwordx4 v[54:57], v[52:53], off sc1
	s_nop 0
	global_load_dwordx4 v[50:53], v[50:51], off offset:16 sc1
	v_add_f32_e32 v83, v83, v60
	global_load_dwordx4 v[58:61], v[58:59], off offset:2048 sc1
	s_nop 0
	global_load_dwordx4 v[62:65], v[62:63], off offset:16 sc1
	v_mov_b32_e32 v92, v85
	v_mov_b32_e32 v93, v84
	s_waitcnt vmcnt(3)
	v_mov_b32_e32 v84, v54
	s_waitcnt vmcnt(1)
	v_mov_b32_e32 v85, v58
	v_pk_mul_f32 v[84:85], v[92:93], v[84:85]
	v_mov_b32_e32 v58, v55
	v_add_f32_e32 v54, v90, v84
	v_add_f32_e32 v90, v54, v85
	v_mov_b32_e32 v84, v50
	s_waitcnt vmcnt(0)
	v_mov_b32_e32 v85, v62
	v_pk_mul_f32 v[84:85], v[92:93], v[84:85]
	v_pk_mul_f32 v[54:55], v[92:93], v[58:59]
	v_add_f32_e32 v50, v89, v84
	v_add_f32_e32 v84, v50, v85
	v_add_f32_e32 v50, v88, v54
	v_mov_b32_e32 v62, v51
	v_add_f32_e32 v54, v50, v55
	v_pk_mul_f32 v[50:51], v[92:93], v[62:63]
	s_nop 0
	v_add_f32_e32 v50, v87, v50
	v_add_f32_e32 v55, v50, v51
	v_mov_b32_e32 v50, v56
	v_mov_b32_e32 v51, v60
	v_pk_mul_f32 v[50:51], v[92:93], v[50:51]
	v_mov_b32_e32 v60, v57
	v_add_f32_e32 v50, v86, v50
	v_add_f32_e32 v56, v50, v51
	v_mov_b32_e32 v50, v52
	v_mov_b32_e32 v51, v64
	v_pk_mul_f32 v[50:51], v[92:93], v[50:51]
	v_mov_b32_e32 v64, v53
	v_add_f32_e32 v50, v81, v50
	v_add_f32_e32 v52, v50, v51
	v_pk_mul_f32 v[50:51], v[92:93], v[60:61]
	v_mov_b32_e32 v81, v99
	v_add_f32_e32 v50, v79, v50
	v_add_f32_e32 v57, v50, v51
	v_pk_mul_f32 v[50:51], v[92:93], v[64:65]
	v_mov_b32_e32 v79, v99
	v_add_f32_e32 v50, v71, v50
	v_add_f32_e32 v50, v50, v51
	v_add_f32_e32 v51, v82, v83
	v_div_scale_f32 v53, s[4:5], v51, v51, 1.0
	v_rcp_f32_e32 v58, v53
	s_nop 0
	v_fma_f32 v59, -v53, v58, 1.0
	v_fmac_f32_e32 v58, v59, v58
	v_div_scale_f32 v59, vcc, 1.0, v51, 1.0
	v_mul_f32_e32 v60, v59, v58
	v_fma_f32 v61, -v53, v60, v59
	v_fmac_f32_e32 v60, v61, v58
	v_fma_f32 v53, -v53, v60, v59
	v_div_fmas_f32 v53, v53, v58, v60
	v_div_fixup_f32 v51, v53, v51, 1.0
	v_mul_f32_e32 v54, v51, v54
	v_mul_f32_e32 v55, v51, v55
	v_mul_f32_e32 v53, v51, v90
	v_mul_f32_e32 v56, v51, v56
	v_mul_f32_e32 v57, v51, v57
	v_mul_f32_e32 v58, v51, v84
	v_mul_f32_e32 v59, v51, v52
	v_mul_f32_e32 v60, v51, v50
	v_cvt_pk_bf16_f32 v50, v53, v54
	v_cvt_pk_bf16_f32 v51, v56, v57
	v_cvt_pk_bf16_f32 v52, v58, v55
	v_lshl_add_u64 v[54:55], v[78:79], 1, s[14:15]
	v_lshl_add_u64 v[54:55], v[54:55], 0, v[80:81]
	v_lshlrev_b32_e32 v56, 1, v70
	v_mov_b32_e32 v57, v99
	v_lshl_add_u64 v[54:55], v[54:55], 0, v[56:57]
	v_add_co_u32_e32 v54, vcc, 0x348b1000, v54
	v_cvt_pk_bf16_f32 v53, v59, v60
	s_nop 1
	v_addc_co_u32_e32 v55, vcc, 0, v55, vcc
	global_store_dwordx4 v[54:55], v[50:53], off offset:512
	s_branch .LBB0_1523

.LBB0_1527:
	v_mov_b32_e32 v1, v0
	s_and_b32 s8, s4, 0x1c0
	s_and_b32 s0, s3, 0xffffff80
	v_ashrrev_i32_e32 v10, 3, v1
	v_add_u32_e32 v4, s8, v10
	v_ashrrev_i32_e32 v5, 31, v4
	v_lshlrev_b64 v[4:5], 15, v[4:5]
	s_ashr_i32 s1, s0, 31
	v_and_b32_e32 v1, 7, v1
	v_lshl_add_u64 v[4:5], s[18:19], 0, v[4:5]
	v_mov_b32_e32 v3, v99
	v_lshlrev_b32_e32 v2, 5, v1
	v_lshl_add_u64 v[4:5], s[0:1], 1, v[4:5]
	v_lshl_add_u64 v[2:3], v[4:5], 0, v[2:3]
	global_load_dwordx4 v[6:9], v[2:3], off sc1
	s_nop 0
	global_load_dwordx4 v[2:5], v[2:3], off offset:16 sc1
	s_movk_i32 s1, 0x204
	v_mul_lo_u32 v11, v10, s1
	v_lshlrev_b32_e32 v12, 6, v1
	v_add3_u32 v14, 0, v11, v12
	v_lshlrev_b32_e32 v98, 4, v1
	v_mul_u32_u24_e32 v1, 0x1020, v1
	v_lshlrev_b32_e32 v13, 2, v10
	s_addk_i32 s0, 0x100
	v_add3_u32 v1, 0, v13, v1
	v_add_u32_e32 v10, s0, v10
	v_add_u32_e32 v15, 0x400, v1
	v_add_u32_e32 v16, 0x800, v1
	v_add_u32_e32 v17, 0xc00, v1
	v_ashrrev_i32_e32 v11, 31, v10
	v_add_u32_e32 v12, 64, v10
	v_lshlrev_b64 v[10:11], 12, v[10:11]
	s_lshl_b32 s62, s8, 1
	v_ashrrev_i32_e32 v13, 31, v12
	v_lshl_add_u64 v[10:11], s[14:15], 0, v[10:11]
	v_lshlrev_b64 v[12:13], 12, v[12:13]
	v_lshl_add_u64 v[10:11], v[10:11], 0, s[62:63]
	v_lshl_add_u64 v[12:13], s[14:15], 0, v[12:13]
	v_lshl_add_u64 v[10:11], v[10:11], 0, v[98:99]
	v_lshl_add_u64 v[12:13], v[12:13], 0, s[62:63]
	v_add_co_u32_e32 v10, vcc, s21, v10
	v_lshl_add_u64 v[12:13], v[12:13], 0, v[98:99]
	s_nop 0
	v_addc_co_u32_e32 v11, vcc, 0, v11, vcc
	v_add_co_u32_e32 v12, vcc, 0x348b1000, v12
	s_add_i32 s5, s5, s72
	s_nop 0
	v_addc_co_u32_e32 v13, vcc, 0, v13, vcc
	s_add_i32 s4, s4, s9
	s_add_i32 s3, s3, s20
	s_cmpk_lt_i32 s5, 0x400
	s_waitcnt vmcnt(1)
	v_lshlrev_b32_e32 v18, 16, v6
	v_and_b32_e32 v6, 0xffff0000, v6
	v_lshlrev_b32_e32 v19, 16, v7
	v_and_b32_e32 v7, 0xffff0000, v7
	v_lshlrev_b32_e32 v20, 16, v8
	v_and_b32_e32 v8, 0xffff0000, v8
	v_lshlrev_b32_e32 v21, 16, v9
	v_and_b32_e32 v9, 0xffff0000, v9
	s_waitcnt vmcnt(0)
	v_lshlrev_b32_e32 v22, 16, v2
	v_and_b32_e32 v2, 0xffff0000, v2
	v_lshlrev_b32_e32 v23, 16, v3
	v_and_b32_e32 v3, 0xffff0000, v3
	v_lshlrev_b32_e32 v24, 16, v4
	v_and_b32_e32 v4, 0xffff0000, v4
	v_lshlrev_b32_e32 v25, 16, v5
	v_and_b32_e32 v5, 0xffff0000, v5
	ds_write2_b32 v14, v18, v6 offset1:1
	ds_write2_b32 v14, v19, v7 offset0:2 offset1:3
	ds_write2_b32 v14, v20, v8 offset0:4 offset1:5
	ds_write2_b32 v14, v21, v9 offset0:6 offset1:7
	ds_write2_b32 v14, v22, v2 offset0:8 offset1:9
	ds_write2_b32 v14, v23, v3 offset0:10 offset1:11
	ds_write2_b32 v14, v24, v4 offset0:12 offset1:13
	ds_write2_b32 v14, v25, v5 offset0:14 offset1:15
	s_waitcnt lgkmcnt(0)
	s_barrier
	ds_read2_b32 v[2:3], v1 offset1:129
	ds_read2_b32 v[4:5], v15 offset0:2 offset1:131
	ds_read2_b32 v[6:7], v16 offset0:4 offset1:133
	ds_read2_b32 v[8:9], v17 offset0:6 offset1:135
	s_waitcnt lgkmcnt(3)
	v_cvt_pk_bf16_f32 v2, v2, v3
	s_waitcnt lgkmcnt(2)
	v_cvt_pk_bf16_f32 v3, v4, v5
	s_waitcnt lgkmcnt(1)
	v_cvt_pk_bf16_f32 v4, v6, v7
	s_waitcnt lgkmcnt(0)
	v_cvt_pk_bf16_f32 v5, v8, v9
	ds_read2_b32 v[6:7], v1 offset0:64 offset1:193
	ds_read2_b32 v[8:9], v15 offset0:66 offset1:195
	ds_read2_b32 v[14:15], v16 offset0:68 offset1:197
	ds_read2_b32 v[16:17], v17 offset0:70 offset1:199
	global_store_dwordx4 v[10:11], v[2:5], off offset:1536
	s_waitcnt lgkmcnt(3)
	s_nop 0
	v_cvt_pk_bf16_f32 v2, v6, v7
	s_waitcnt lgkmcnt(2)
	v_cvt_pk_bf16_f32 v3, v8, v9
	s_waitcnt lgkmcnt(1)
	v_cvt_pk_bf16_f32 v4, v14, v15
	s_waitcnt lgkmcnt(0)
	v_cvt_pk_bf16_f32 v5, v16, v17
	global_store_dwordx4 v[12:13], v[2:5], off offset:1536
	s_waitcnt lgkmcnt(0)
	s_barrier
	s_cbranch_scc1 .LBB0_1527

.LBB0_1673:
	s_or_b64 exec, exec, s[4:5]
	s_mov_b64 s[24:25], exec
	v_mbcnt_lo_u32_b32 v1, s24, 0
	v_mbcnt_hi_u32_b32 v1, s25, v1
	v_cmp_eq_u32_e32 vcc, 0, v1
	s_waitcnt vmcnt(0)
	s_and_saveexec_b64 s[26:27], vcc
	s_cbranch_execz .LBB0_1675
	s_bcnt1_i32_b64 s3, s[24:25]
	v_mov_b32_e32 v1, s3
	v_mov_b32_e32 v2, 0x2000
	global_atomic_add v2, v1, s[22:23] offset:1024

.LBB0_1676:
	s_or_b64 exec, exec, s[0:1]
	v_readlane_b32 s4, v255, 46
	v_readlane_b32 s5, v255, 47
	v_mov_b32_e32 v108, v0
	s_waitcnt lgkmcnt(0)
	v_cndmask_b32_e64 v1, 0, 1, s[4:5]
	s_barrier
	v_cmp_ne_u32_e64 s[0:1], 1, v1
	s_andn2_b64 vcc, exec, s[4:5]
	v_cmp_gt_i32_e64 s[22:23], 8, v108
	s_cbranch_vccnz .LBB0_1680
	s_and_saveexec_b64 s[24:25], s[22:23]
	v_lshl_add_u32 v1, v108, 2, 0
	ds_write_b32 v1, v99
	s_or_b64 exec, exec, s[24:25]
	v_lshlrev_b32_e32 v1, 4, v108
	v_readlane_b32 s36, v251, 57
	v_ashrrev_i32_e32 v2, 1, v108
	v_and_b32_e32 v98, 16, v1
	v_readlane_b32 s50, v252, 7
	v_readlane_b32 s51, v252, 8
	v_ashrrev_i32_e32 v3, 31, v2
	v_lshlrev_b64 v[2:3], 5, v[2:3]
	v_lshl_add_u64 v[6:7], s[50:51], 0, v[98:99]
	v_lshl_add_u64 v[2:3], v[6:7], 0, v[2:3]
	global_load_dwordx4 v[2:5], v[2:3], off sc1
	v_lshlrev_b32_e32 v1, 13, v108
	v_and_b32_e32 v1, 0xe000, v1
	v_lshlrev_b32_e32 v8, 1, v108
	v_add_u32_e32 v1, 0, v1
	v_and_b32_e32 v8, -16, v8
	v_add_u32_e32 v8, v1, v8
	v_readlane_b32 s37, v251, 58
	v_readlane_b32 s38, v251, 59
	v_readlane_b32 s39, v251, 60
	v_readlane_b32 s40, v251, 61
	v_readlane_b32 s41, v251, 62
	v_readlane_b32 s42, v251, 63
	v_readlane_b32 s43, v252, 0
	v_readlane_b32 s44, v252, 1
	v_readlane_b32 s45, v252, 2
	v_readlane_b32 s46, v252, 3
	v_readlane_b32 s47, v252, 4
	v_readlane_b32 s48, v252, 5
	v_readlane_b32 s49, v252, 6
	s_waitcnt vmcnt(0)
	ds_write_b128 v8, v[2:5] offset:4096
	v_add_u32_e32 v8, 0x200, v108
	v_ashrrev_i32_e32 v2, 1, v8
	v_ashrrev_i32_e32 v3, 31, v2
	v_lshlrev_b64 v[2:3], 5, v[2:3]
	v_lshl_add_u64 v[2:3], v[6:7], 0, v[2:3]
	global_load_dwordx4 v[2:5], v[2:3], off sc1
	v_lshlrev_b32_e32 v8, 1, v8
	v_and_b32_e32 v8, -16, v8
	v_add_u32_e32 v8, v1, v8
	s_waitcnt vmcnt(0)
	ds_write_b128 v8, v[2:5] offset:4096
	v_add_u32_e32 v8, 0x400, v108
	v_ashrrev_i32_e32 v2, 1, v8
	v_ashrrev_i32_e32 v3, 31, v2
	v_lshlrev_b64 v[2:3], 5, v[2:3]
	v_lshl_add_u64 v[2:3], v[6:7], 0, v[2:3]
	global_load_dwordx4 v[2:5], v[2:3], off sc1
	v_lshlrev_b32_e32 v8, 1, v8
	v_and_b32_e32 v8, -16, v8
	v_add_u32_e32 v8, v1, v8
	s_waitcnt vmcnt(0)
	ds_write_b128 v8, v[2:5] offset:4096
	v_add_u32_e32 v8, 0x600, v108
	v_ashrrev_i32_e32 v2, 1, v8
	v_ashrrev_i32_e32 v3, 31, v2
	v_lshlrev_b64 v[2:3], 5, v[2:3]
	v_lshl_add_u64 v[2:3], v[6:7], 0, v[2:3]
	global_load_dwordx4 v[2:5], v[2:3], off sc1
	v_lshlrev_b32_e32 v8, 1, v8
	v_and_b32_e32 v8, -16, v8
	v_add_u32_e32 v8, v1, v8
	s_waitcnt vmcnt(0)
	ds_write_b128 v8, v[2:5] offset:4096
	v_add_u32_e32 v8, 0x800, v108
	v_ashrrev_i32_e32 v2, 1, v8
	v_ashrrev_i32_e32 v3, 31, v2
	v_lshlrev_b64 v[2:3], 5, v[2:3]
	v_lshl_add_u64 v[2:3], v[6:7], 0, v[2:3]
	global_load_dwordx4 v[2:5], v[2:3], off sc1
	v_lshlrev_b32_e32 v8, 1, v8
	v_and_b32_e32 v8, -16, v8
	v_add_u32_e32 v8, v1, v8
	s_waitcnt vmcnt(0)
	ds_write_b128 v8, v[2:5] offset:4096
	v_add_u32_e32 v8, 0xa00, v108
	v_ashrrev_i32_e32 v2, 1, v8
	v_ashrrev_i32_e32 v3, 31, v2
	v_lshlrev_b64 v[2:3], 5, v[2:3]
	v_lshl_add_u64 v[2:3], v[6:7], 0, v[2:3]
	global_load_dwordx4 v[2:5], v[2:3], off sc1
	v_lshlrev_b32_e32 v8, 1, v8
	v_and_b32_e32 v8, -16, v8
	v_add_u32_e32 v8, v1, v8
	s_waitcnt vmcnt(0)
	ds_write_b128 v8, v[2:5] offset:4096
	v_add_u32_e32 v8, 0xc00, v108
	v_ashrrev_i32_e32 v2, 1, v8
	v_ashrrev_i32_e32 v3, 31, v2
	v_lshlrev_b64 v[2:3], 5, v[2:3]
	v_lshl_add_u64 v[2:3], v[6:7], 0, v[2:3]
	global_load_dwordx4 v[2:5], v[2:3], off sc1
	v_lshlrev_b32_e32 v8, 1, v8
	v_and_b32_e32 v8, -16, v8
	v_add_u32_e32 v8, v1, v8
	s_waitcnt vmcnt(0)
	ds_write_b128 v8, v[2:5] offset:4096
	v_add_u32_e32 v8, 0xe00, v108
	v_ashrrev_i32_e32 v2, 1, v8
	v_ashrrev_i32_e32 v3, 31, v2
	v_lshlrev_b64 v[2:3], 5, v[2:3]
	v_lshl_add_u64 v[2:3], v[6:7], 0, v[2:3]
	global_load_dwordx4 v[2:5], v[2:3], off sc1
	v_lshlrev_b32_e32 v6, 1, v8
	v_and_b32_e32 v6, -16, v6
	v_add_u32_e32 v1, v1, v6
	s_waitcnt vmcnt(0)
	ds_write_b128 v1, v[2:5] offset:4096
	s_waitcnt lgkmcnt(0)
	s_barrier

.LBB0_1685:
	v_readlane_b32 s40, v251, 9
	v_cmp_gt_i32_e64 s[24:25], s57, v110
	v_readlane_b32 s45, v251, 14
	v_mov_b32_e32 v4, s77
	v_readlane_b32 s44, v251, 13
	v_mov_b32_e32 v5, s45
	s_and_b64 s[26:27], s[70:71], s[24:25]
	v_ashrrev_i32_e32 v111, 31, v110
	v_cndmask_b32_e64 v5, v4, v5, s[26:27]
	v_mov_b32_e32 v4, s76
	v_mov_b32_e32 v6, s44
	v_lshlrev_b64 v[2:3], 13, v[110:111]
	v_cndmask_b32_e64 v4, v4, v6, s[26:27]
	v_lshl_add_u64 v[26:27], v[4:5], 0, v[2:3]
	v_lshlrev_b32_e32 v38, 2, v112
	v_mov_b32_e32 v39, v99
	v_lshl_add_u64 v[14:15], v[26:27], 0, v[38:39]
	global_load_dwordx4 v[2:5], v[14:15], off sc1
	v_lshlrev_b64 v[198:199], 11, v[110:111]
	s_mov_b64 s[30:31], s[70:71]
	v_lshlrev_b64 v[34:35], 2, v[198:199]
	v_readlane_b32 s41, v251, 10
	v_readlane_b32 s42, v251, 11
	v_readlane_b32 s43, v251, 12
	v_readlane_b32 s46, v251, 15
	v_readlane_b32 s47, v251, 16
	v_readlane_b32 s48, v251, 17
	v_readlane_b32 s49, v251, 18
	v_readlane_b32 s50, v251, 19
	v_readlane_b32 s51, v251, 20
	v_readlane_b32 s52, v251, 21
	v_readlane_b32 s53, v251, 22
	v_readlane_b32 s54, v251, 23
	v_readlane_b32 s55, v251, 24
	s_and_saveexec_b64 s[28:29], s[26:27]
	s_cbranch_execz .LBB0_1687
	v_lshl_add_u64 v[10:11], v[148:149], 0, v[34:35]
	s_waitcnt lgkmcnt(2)
	global_load_dwordx4 v[6:9], v[10:11], off sc1
	s_waitcnt vmcnt(0) lgkmcnt(0)
	v_pk_add_f32 v[16:17], v[6:7], 0 op_sel_hi:[1,0]
	v_add_co_u32_e32 v6, vcc, 0x200000, v10
	v_pk_add_f32 v[12:13], v[8:9], 0 op_sel_hi:[1,0]
	s_nop 0
	v_addc_co_u32_e32 v7, vcc, 0, v11, vcc
	global_load_dwordx4 v[6:9], v[6:7], off sc1
	s_waitcnt vmcnt(0)
	v_pk_add_f32 v[16:17], v[16:17], v[6:7]
	v_add_co_u32_e32 v6, vcc, 0x400000, v10
	v_pk_add_f32 v[12:13], v[12:13], v[8:9]
	s_nop 0
	v_addc_co_u32_e32 v7, vcc, 0, v11, vcc
	global_load_dwordx4 v[6:9], v[6:7], off sc1
	s_waitcnt vmcnt(0)
	v_pk_add_f32 v[16:17], v[16:17], v[6:7]
	v_add_co_u32_e32 v6, vcc, 0x600000, v10
	v_pk_add_f32 v[12:13], v[12:13], v[8:9]
	s_nop 0
	v_addc_co_u32_e32 v7, vcc, 0, v11, vcc
	global_load_dwordx4 v[6:9], v[6:7], off sc1
	s_waitcnt vmcnt(0)
	v_pk_add_f32 v[10:11], v[12:13], v[8:9]
	v_pk_add_f32 v[12:13], v[16:17], v[6:7]
	global_load_dwordx4 v[6:9], v[150:151], off sc1
	s_waitcnt vmcnt(0)
	v_pk_fma_f32 v[4:5], v[10:11], v[8:9], v[4:5]
	v_pk_fma_f32 v[2:3], v[12:13], v[6:7], v[2:3]
	v_lshl_add_u64 v[6:7], v[138:139], 0, v[34:35]
	global_store_dwordx4 v[6:7], v[2:5], off
.LBB0_1687:
	s_or_b64 exec, exec, s[28:29]
	s_waitcnt lgkmcnt(2)
	global_load_dwordx4 v[6:9], v[14:15], off offset:1024 sc1
	s_and_saveexec_b64 s[28:29], s[26:27]
	v_readlane_b32 s18, v255, 43
	v_readlane_b32 s19, v255, 44
	s_cbranch_execz .LBB0_1689
	s_waitcnt lgkmcnt(0)
	v_lshl_add_u64 v[16:17], v[174:175], 0, v[34:35]
	global_load_dwordx4 v[10:13], v[16:17], off sc1
	s_waitcnt vmcnt(0)
	v_pk_add_f32 v[20:21], v[10:11], 0 op_sel_hi:[1,0]
	v_add_co_u32_e32 v10, vcc, 0x200000, v16
	v_pk_add_f32 v[18:19], v[12:13], 0 op_sel_hi:[1,0]
	s_nop 0
	v_addc_co_u32_e32 v11, vcc, 0, v17, vcc
	global_load_dwordx4 v[10:13], v[10:11], off sc1
	s_waitcnt vmcnt(0)
	v_pk_add_f32 v[20:21], v[20:21], v[10:11]
	v_add_co_u32_e32 v10, vcc, 0x400000, v16
	v_pk_add_f32 v[18:19], v[18:19], v[12:13]
	s_nop 0
	v_addc_co_u32_e32 v11, vcc, 0, v17, vcc
	global_load_dwordx4 v[10:13], v[10:11], off sc1
	s_waitcnt vmcnt(0)
	v_pk_add_f32 v[20:21], v[20:21], v[10:11]
	v_add_co_u32_e32 v10, vcc, 0x600000, v16
	v_pk_add_f32 v[18:19], v[18:19], v[12:13]
	s_nop 0
	v_addc_co_u32_e32 v11, vcc, 0, v17, vcc
	global_load_dwordx4 v[10:13], v[10:11], off sc1
	s_waitcnt vmcnt(0)
	v_pk_add_f32 v[16:17], v[18:19], v[12:13]
	v_pk_add_f32 v[18:19], v[20:21], v[10:11]
	global_load_dwordx4 v[10:13], v[152:153], off sc1
	s_waitcnt vmcnt(0)
	v_pk_fma_f32 v[8:9], v[16:17], v[12:13], v[8:9]
	v_pk_fma_f32 v[6:7], v[18:19], v[10:11], v[6:7]
	v_lshl_add_u64 v[10:11], v[180:181], 0, v[34:35]
	global_store_dwordx4 v[10:11], v[6:9], off
.LBB0_1689:
	s_or_b64 exec, exec, s[28:29]
	global_load_dwordx4 v[10:13], v[14:15], off offset:2048 sc1
	s_and_saveexec_b64 s[28:29], s[26:27]
	v_readlane_b32 s20, v253, 39
	v_readlane_b32 s21, v253, 40
	s_cbranch_execz .LBB0_1691
	v_lshl_add_u64 v[20:21], v[182:183], 0, v[34:35]
	s_waitcnt lgkmcnt(0)
	global_load_dwordx4 v[16:19], v[20:21], off sc1
	s_waitcnt vmcnt(0)
	v_pk_add_f32 v[24:25], v[16:17], 0 op_sel_hi:[1,0]
	v_add_co_u32_e32 v16, vcc, 0x200000, v20
	v_pk_add_f32 v[22:23], v[18:19], 0 op_sel_hi:[1,0]
	s_nop 0
	v_addc_co_u32_e32 v17, vcc, 0, v21, vcc
	global_load_dwordx4 v[16:19], v[16:17], off sc1
	s_waitcnt vmcnt(0)
	v_pk_add_f32 v[24:25], v[24:25], v[16:17]
	v_add_co_u32_e32 v16, vcc, 0x400000, v20
	v_pk_add_f32 v[22:23], v[22:23], v[18:19]
	s_nop 0
	v_addc_co_u32_e32 v17, vcc, 0, v21, vcc
	global_load_dwordx4 v[16:19], v[16:17], off sc1
	s_waitcnt vmcnt(0)
	v_pk_add_f32 v[24:25], v[24:25], v[16:17]
	v_add_co_u32_e32 v16, vcc, 0x600000, v20
	v_pk_add_f32 v[22:23], v[22:23], v[18:19]
	s_nop 0
	v_addc_co_u32_e32 v17, vcc, 0, v21, vcc
	global_load_dwordx4 v[16:19], v[16:17], off sc1
	s_waitcnt vmcnt(0)
	v_pk_add_f32 v[20:21], v[22:23], v[18:19]
	v_pk_add_f32 v[22:23], v[24:25], v[16:17]
	global_load_dwordx4 v[16:19], v[154:155], off sc1
	s_waitcnt vmcnt(0)
	v_pk_fma_f32 v[12:13], v[20:21], v[18:19], v[12:13]
	v_pk_fma_f32 v[10:11], v[22:23], v[16:17], v[10:11]
	v_lshl_add_u64 v[16:17], v[184:185], 0, v[34:35]
	global_store_dwordx4 v[16:17], v[10:13], off
.LBB0_1691:
	s_or_b64 exec, exec, s[28:29]
	s_waitcnt lgkmcnt(0)
	global_load_dwordx4 v[14:17], v[14:15], off offset:3072 sc1
	s_and_saveexec_b64 s[28:29], s[26:27]
	s_cbranch_execz .LBB0_1693
	v_lshl_add_u64 v[22:23], v[186:187], 0, v[34:35]
	global_load_dwordx4 v[18:21], v[22:23], off sc1
	s_waitcnt vmcnt(0)
	v_pk_add_f32 v[28:29], v[18:19], 0 op_sel_hi:[1,0]
	v_add_co_u32_e32 v18, vcc, 0x200000, v22
	v_pk_add_f32 v[24:25], v[20:21], 0 op_sel_hi:[1,0]
	s_nop 0
	v_addc_co_u32_e32 v19, vcc, 0, v23, vcc
	global_load_dwordx4 v[18:21], v[18:19], off sc1
	s_waitcnt vmcnt(0)
	v_pk_add_f32 v[28:29], v[28:29], v[18:19]
	v_add_co_u32_e32 v18, vcc, 0x400000, v22
	v_pk_add_f32 v[24:25], v[24:25], v[20:21]
	s_nop 0
	v_addc_co_u32_e32 v19, vcc, 0, v23, vcc
	global_load_dwordx4 v[18:21], v[18:19], off sc1
	s_waitcnt vmcnt(0)
	v_pk_add_f32 v[28:29], v[28:29], v[18:19]
	v_add_co_u32_e32 v18, vcc, 0x600000, v22
	v_pk_add_f32 v[24:25], v[24:25], v[20:21]
	s_nop 0
	v_addc_co_u32_e32 v19, vcc, 0, v23, vcc
	global_load_dwordx4 v[18:21], v[18:19], off sc1
	s_waitcnt vmcnt(0)
	v_pk_add_f32 v[22:23], v[24:25], v[20:21]
	v_pk_add_f32 v[24:25], v[28:29], v[18:19]
	global_load_dwordx4 v[18:21], v[156:157], off sc1
	s_waitcnt vmcnt(0)
	v_pk_fma_f32 v[16:17], v[22:23], v[20:21], v[16:17]
	v_pk_fma_f32 v[14:15], v[24:25], v[18:19], v[14:15]
	v_lshl_add_u64 v[18:19], v[188:189], 0, v[34:35]
	global_store_dwordx4 v[18:19], v[14:17], off
.LBB0_1693:
	s_or_b64 exec, exec, s[28:29]
	v_lshlrev_b32_e32 v82, 2, v120
	v_mov_b32_e32 v83, v99
	v_lshl_add_u64 v[18:19], v[26:27], 0, v[82:83]
	global_load_dwordx4 v[18:21], v[18:19], off sc1
	s_and_saveexec_b64 s[28:29], s[26:27]
	s_cbranch_execz .LBB0_1695
	v_lshl_add_u64 v[28:29], v[158:159], 0, v[34:35]
	global_load_dwordx4 v[22:25], v[28:29], off sc1
	s_waitcnt vmcnt(0)
	v_pk_add_f32 v[32:33], v[22:23], 0 op_sel_hi:[1,0]
	v_add_co_u32_e32 v22, vcc, 0x200000, v28
	v_pk_add_f32 v[30:31], v[24:25], 0 op_sel_hi:[1,0]
	s_nop 0
	v_addc_co_u32_e32 v23, vcc, 0, v29, vcc
	global_load_dwordx4 v[22:25], v[22:23], off sc1
	s_waitcnt vmcnt(0)
	v_pk_add_f32 v[32:33], v[32:33], v[22:23]
	v_add_co_u32_e32 v22, vcc, 0x400000, v28
	v_pk_add_f32 v[30:31], v[30:31], v[24:25]
	s_nop 0
	v_addc_co_u32_e32 v23, vcc, 0, v29, vcc
	global_load_dwordx4 v[22:25], v[22:23], off sc1
	s_waitcnt vmcnt(0)
	v_pk_add_f32 v[32:33], v[32:33], v[22:23]
	v_add_co_u32_e32 v22, vcc, 0x600000, v28
	v_pk_add_f32 v[30:31], v[30:31], v[24:25]
	s_nop 0
	v_addc_co_u32_e32 v23, vcc, 0, v29, vcc
	global_load_dwordx4 v[22:25], v[22:23], off sc1
	s_waitcnt vmcnt(0)
	v_pk_add_f32 v[28:29], v[30:31], v[24:25]
	v_pk_add_f32 v[30:31], v[32:33], v[22:23]
	global_load_dwordx4 v[22:25], v[160:161], off sc1
	s_waitcnt vmcnt(0)
	v_pk_fma_f32 v[20:21], v[28:29], v[24:25], v[20:21]
	v_pk_fma_f32 v[18:19], v[30:31], v[22:23], v[18:19]
	v_lshl_add_u64 v[22:23], v[140:141], 0, v[34:35]
	global_store_dwordx4 v[22:23], v[18:21], off
.LBB0_1695:
	s_or_b64 exec, exec, s[28:29]
	v_lshlrev_b32_e32 v84, 2, v122
	v_mov_b32_e32 v85, v99
	v_lshl_add_u64 v[22:23], v[26:27], 0, v[84:85]
	global_load_dwordx4 v[22:25], v[22:23], off sc1
	s_and_saveexec_b64 s[28:29], s[26:27]
	s_cbranch_execz .LBB0_1697
	v_lshl_add_u64 v[32:33], v[162:163], 0, v[34:35]
	global_load_dwordx4 v[28:31], v[32:33], off sc1
	s_waitcnt vmcnt(0)
	v_pk_add_f32 v[40:41], v[28:29], 0 op_sel_hi:[1,0]
	v_add_co_u32_e32 v28, vcc, 0x200000, v32
	v_pk_add_f32 v[36:37], v[30:31], 0 op_sel_hi:[1,0]
	s_nop 0
	v_addc_co_u32_e32 v29, vcc, 0, v33, vcc
	global_load_dwordx4 v[28:31], v[28:29], off sc1
	s_waitcnt vmcnt(0)
	v_pk_add_f32 v[40:41], v[40:41], v[28:29]
	v_add_co_u32_e32 v28, vcc, 0x400000, v32
	v_pk_add_f32 v[36:37], v[36:37], v[30:31]
	s_nop 0
	v_addc_co_u32_e32 v29, vcc, 0, v33, vcc
	global_load_dwordx4 v[28:31], v[28:29], off sc1
	s_waitcnt vmcnt(0)
	v_pk_add_f32 v[40:41], v[40:41], v[28:29]
	v_add_co_u32_e32 v28, vcc, 0x600000, v32
	v_pk_add_f32 v[36:37], v[36:37], v[30:31]
	s_nop 0
	v_addc_co_u32_e32 v29, vcc, 0, v33, vcc
	global_load_dwordx4 v[28:31], v[28:29], off sc1
	s_waitcnt vmcnt(0)
	v_pk_add_f32 v[32:33], v[36:37], v[30:31]
	v_pk_add_f32 v[36:37], v[40:41], v[28:29]
	global_load_dwordx4 v[28:31], v[164:165], off sc1
	s_waitcnt vmcnt(0)
	v_pk_fma_f32 v[24:25], v[32:33], v[30:31], v[24:25]
	v_pk_fma_f32 v[22:23], v[36:37], v[28:29], v[22:23]
	v_lshl_add_u64 v[28:29], v[142:143], 0, v[34:35]
	global_store_dwordx4 v[28:29], v[22:25], off
.LBB0_1697:
	s_or_b64 exec, exec, s[28:29]
	v_lshlrev_b32_e32 v86, 2, v124
	v_mov_b32_e32 v87, v99
	v_lshl_add_u64 v[28:29], v[26:27], 0, v[86:87]
	global_load_dwordx4 v[30:33], v[28:29], off sc1
	s_and_saveexec_b64 s[28:29], s[26:27]
	s_cbranch_execz .LBB0_1699
	v_lshl_add_u64 v[28:29], v[166:167], 0, v[34:35]
	global_load_dwordx4 v[40:43], v[28:29], off sc1
	s_waitcnt vmcnt(0)
	v_pk_add_f32 v[44:45], v[40:41], 0 op_sel_hi:[1,0]
	v_add_co_u32_e32 v40, vcc, 0x200000, v28
	v_pk_add_f32 v[36:37], v[42:43], 0 op_sel_hi:[1,0]
	s_nop 0
	v_addc_co_u32_e32 v41, vcc, 0, v29, vcc
	global_load_dwordx4 v[40:43], v[40:41], off sc1
	s_waitcnt vmcnt(0)
	v_pk_add_f32 v[44:45], v[44:45], v[40:41]
	v_add_co_u32_e32 v40, vcc, 0x400000, v28
	v_pk_add_f32 v[36:37], v[36:37], v[42:43]
	s_nop 0
	v_addc_co_u32_e32 v41, vcc, 0, v29, vcc
	global_load_dwordx4 v[40:43], v[40:41], off sc1
	v_add_co_u32_e32 v28, vcc, 0x600000, v28
	s_waitcnt vmcnt(0)
	v_pk_add_f32 v[36:37], v[36:37], v[42:43]
	v_addc_co_u32_e32 v29, vcc, 0, v29, vcc
	v_pk_add_f32 v[44:45], v[44:45], v[40:41]
	global_load_dwordx4 v[40:43], v[28:29], off sc1
	s_waitcnt vmcnt(0)
	v_pk_add_f32 v[28:29], v[36:37], v[42:43]
	v_pk_add_f32 v[36:37], v[44:45], v[40:41]
	global_load_dwordx4 v[40:43], v[168:169], off sc1
	s_waitcnt vmcnt(0)
	v_pk_fma_f32 v[32:33], v[28:29], v[42:43], v[32:33]
	v_pk_fma_f32 v[30:31], v[36:37], v[40:41], v[30:31]
	v_lshl_add_u64 v[28:29], v[144:145], 0, v[34:35]
	global_store_dwordx4 v[28:29], v[30:33], off
.LBB0_1699:
	s_or_b64 exec, exec, s[28:29]
	v_lshlrev_b32_e32 v98, 2, v126
	v_lshl_add_u64 v[26:27], v[26:27], 0, v[98:99]
	global_load_dwordx4 v[26:29], v[26:27], off sc1
	s_and_saveexec_b64 s[28:29], s[26:27]
	s_cbranch_execz .LBB0_1701
	v_lshl_add_u64 v[36:37], v[170:171], 0, v[34:35]
	global_load_dwordx4 v[40:43], v[36:37], off sc1
	v_lshl_add_u64 v[34:35], v[146:147], 0, v[34:35]
	s_waitcnt vmcnt(0)
	v_pk_add_f32 v[46:47], v[40:41], 0 op_sel_hi:[1,0]
	v_add_co_u32_e32 v40, vcc, 0x200000, v36
	v_pk_add_f32 v[44:45], v[42:43], 0 op_sel_hi:[1,0]
	s_nop 0
	v_addc_co_u32_e32 v41, vcc, 0, v37, vcc
	global_load_dwordx4 v[40:43], v[40:41], off sc1
	s_waitcnt vmcnt(0)
	v_pk_add_f32 v[46:47], v[46:47], v[40:41]
	v_add_co_u32_e32 v40, vcc, 0x400000, v36
	v_pk_add_f32 v[44:45], v[44:45], v[42:43]
	s_nop 0
	v_addc_co_u32_e32 v41, vcc, 0, v37, vcc
	global_load_dwordx4 v[40:43], v[40:41], off sc1
	v_add_co_u32_e32 v36, vcc, 0x600000, v36
	s_waitcnt vmcnt(0)
	v_pk_add_f32 v[44:45], v[44:45], v[42:43]
	v_addc_co_u32_e32 v37, vcc, 0, v37, vcc
	v_pk_add_f32 v[46:47], v[46:47], v[40:41]
	global_load_dwordx4 v[40:43], v[36:37], off sc1
	s_waitcnt vmcnt(0)
	v_pk_add_f32 v[36:37], v[44:45], v[42:43]
	v_pk_add_f32 v[44:45], v[46:47], v[40:41]
	global_load_dwordx4 v[40:43], v[172:173], off sc1
	s_waitcnt vmcnt(0)
	v_pk_fma_f32 v[28:29], v[36:37], v[42:43], v[28:29]
	v_pk_fma_f32 v[26:27], v[44:45], v[40:41], v[26:27]
	global_store_dwordx4 v[34:35], v[26:29], off

.LBB0_1942:
	s_or_b64 exec, exec, s[0:1]
	v_readlane_b32 s0, v253, 43
	v_readlane_b32 s1, v253, 44
	s_waitcnt lgkmcnt(0)
	s_barrier
	s_nop 2
	global_load_dwordx4 v[2:5], v99, s[0:1] offset:16 sc1
	global_load_dwordx4 v[6:9], v99, s[0:1] sc1
	v_readlane_b32 s0, v255, 28
	s_waitcnt vmcnt(0)
	v_add_u32_e32 v1, 0xff, v7
	v_and_b32_e32 v1, 0xffffff00, v1
	v_add_u32_e32 v1, v6, v1
	v_add_u32_e32 v1, 0xff, v1
	v_and_b32_e32 v1, 0xffffff00, v1
	v_add_u32_e32 v1, v8, v1
	v_add_u32_e32 v1, 0xff, v1
	v_and_b32_e32 v1, 0xffffff00, v1
	v_add_u32_e32 v1, v9, v1
	v_add_u32_e32 v1, 0xff, v1
	v_and_b32_e32 v1, 0xffffff00, v1
	v_add_u32_e32 v1, v2, v1
	v_add_u32_e32 v1, 0xff, v1
	v_and_b32_e32 v1, 0xffffff00, v1
	v_add_u32_e32 v1, v3, v1
	v_add_u32_e32 v1, 0xff, v1
	v_and_b32_e32 v1, 0xffffff00, v1
	v_add_u32_e32 v1, v4, v1
	v_add_u32_e32 v1, 0xff, v1
	v_and_b32_e32 v1, 0xffffff00, v1
	v_add_u32_e32 v1, v5, v1
	v_mov_b32_e32 v2, v0
	v_add_u32_e32 v1, 0xff, v1
	v_and_b32_e32 v1, 0xffffff00, v1
	v_ashrrev_i32_e32 v3, 6, v2
	v_add_u32_e32 v42, s0, v3
	v_cmp_lt_i32_e32 vcc, v42, v1
	s_and_saveexec_b64 s[22:23], vcc
	v_readlane_b32 s70, v252, 21
	v_readlane_b32 s71, v252, 22
	s_cbranch_execz .LBB0_1947
	v_and_b32_e32 v2, 63, v2
	v_lshlrev_b32_e32 v44, 3, v2
	v_cmp_eq_u32_e64 s[0:1], 0, v2
	v_or_b32_e32 v2, 0x800, v44
	v_or_b32_e32 v4, 0xa00, v44
	v_or_b32_e32 v6, 0xc00, v44
	v_or_b32_e32 v8, 0xe00, v44
	v_mov_b32_e32 v45, v99
	v_or_b32_e32 v46, 0x1000, v44
	v_mov_b32_e32 v47, v99
	v_or_b32_e32 v48, 0x1200, v44
	v_mov_b32_e32 v49, v99
	v_or_b32_e32 v50, 0x1400, v44
	v_mov_b32_e32 v51, v99
	s_mov_b64 s[24:25], 0
	v_lshlrev_b32_e32 v52, 1, v2
	v_lshlrev_b32_e32 v54, 1, v4
	v_lshlrev_b32_e32 v56, 1, v6
	v_lshlrev_b32_e32 v58, 1, v8
	s_branch .LBB0_1945

.LBB0_1945:
	v_readlane_b32 s4, v253, 57
	v_ashrrev_i32_e32 v43, 31, v42
	v_readlane_b32 s5, v253, 58
	s_movk_i32 s3, 0x2c00
	v_lshlrev_b32_e32 v98, 1, v44
	v_lshl_add_u64 v[60:61], v[42:43], 2, s[4:5]
	global_load_dword v2, v[60:61], off sc1
	v_readlane_b32 s4, v254, 13
	v_readlane_b32 s5, v254, 14
	v_mov_b32_e32 v53, v99
	v_mov_b32_e32 v55, v99
	v_mov_b32_e32 v57, v99
	v_mov_b32_e32 v59, v99
	s_waitcnt vmcnt(0)
	v_max_f32_e32 v2, v2, v2
	v_max_f32_e32 v43, 0x1e3ce508, v2
	v_mov_b64_e32 v[2:3], s[4:5]
	v_mad_i64_i32 v[2:3], s[4:5], v42, s3, v[2:3]
	v_lshl_add_u64 v[4:5], v[2:3], 0, v[98:99]
	global_load_dwordx4 v[64:67], v[4:5], off sc1
	global_load_dwordx4 v[38:41], v[4:5], off offset:1024 sc1
	global_load_dwordx4 v[34:37], v[4:5], off offset:2048 sc1
	global_load_dwordx4 v[30:33], v[4:5], off offset:3072 sc1
	s_mov_b32 s3, 0x42fe0000
	v_lshl_add_u64 v[4:5], v[2:3], 0, v[52:53]
	v_div_scale_f32 v53, s[4:5], v43, v43, s3
	global_load_dwordx4 v[26:29], v[4:5], off sc1
	v_lshl_add_u64 v[4:5], v[2:3], 0, v[54:55]
	v_rcp_f32_e32 v55, v53
	global_load_dwordx4 v[22:25], v[4:5], off sc1
	v_lshl_add_u64 v[4:5], v[2:3], 0, v[56:57]
	global_load_dwordx4 v[18:21], v[4:5], off sc1
	v_fma_f32 v57, -v53, v55, 1.0
	v_fmac_f32_e32 v55, v57, v55
	v_div_scale_f32 v57, vcc, s3, v43, s3
	v_lshl_add_u64 v[4:5], v[2:3], 0, v[58:59]
	v_mul_f32_e32 v59, v57, v55
	v_fma_f32 v62, -v53, v59, v57
	v_fmac_f32_e32 v59, v62, v55
	v_fma_f32 v53, -v53, v59, v57
	v_div_fmas_f32 v53, v53, v55, v59
	v_div_fixup_f32 v53, v53, v43, s3
	v_lshlrev_b32_e32 v98, 1, v46
	global_load_dwordx4 v[14:17], v[4:5], off sc1
	v_lshl_add_u64 v[4:5], v[2:3], 0, v[98:99]
	v_lshlrev_b32_e32 v98, 1, v48
	v_mov_b64_e32 v[62:63], s[18:19]
	s_movk_i32 s3, 0x1600
	global_load_dwordx4 v[10:13], v[4:5], off sc1
	v_lshl_add_u64 v[4:5], v[2:3], 0, v[98:99]
	v_lshlrev_b32_e32 v98, 1, v50
	v_mad_i64_i32 v[62:63], s[4:5], v42, s3, v[62:63]
	v_lshl_add_u64 v[2:3], v[2:3], 0, v[98:99]
	global_load_dwordx4 v[6:9], v[4:5], off sc1
	s_waitcnt vmcnt(9)
	v_lshlrev_b32_e32 v55, 16, v64
	v_and_b32_e32 v57, 0xffff0000, v64
	v_lshlrev_b32_e32 v59, 16, v65
	v_and_b32_e32 v64, 0xffff0000, v65
	v_lshlrev_b32_e32 v65, 16, v66
	v_and_b32_e32 v66, 0xffff0000, v66
	v_mul_f32_e32 v66, v53, v66
	v_rndne_f32_e32 v66, v66
	v_cvt_i32_f32_e32 v66, v66
	v_mul_f32_e32 v57, v53, v57
	v_lshlrev_b32_e32 v68, 16, v67
	v_mul_f32_e32 v55, v53, v55
	v_rndne_f32_e32 v57, v57
	v_lshlrev_b32_e32 v66, 8, v66
	v_mul_f32_e32 v59, v53, v59
	v_mul_f32_e32 v64, v53, v64
	v_rndne_f32_e32 v55, v55
	v_cvt_i32_f32_e32 v57, v57
	v_and_b32_e32 v69, 0xff00, v66
	v_rndne_f32_e32 v59, v59
	v_mul_f32_e32 v66, v53, v68
	v_rndne_f32_e32 v64, v64
	v_cvt_i32_f32_e32 v55, v55
	v_cvt_i32_f32_sdwa v59, v59 dst_sel:WORD_1 dst_unused:UNUSED_PAD src0_sel:DWORD
	v_rndne_f32_e32 v66, v66
	v_cvt_i32_f32_e32 v64, v64
	v_cvt_i32_f32_sdwa v66, v66 dst_sel:WORD_1 dst_unused:UNUSED_PAD src0_sel:DWORD
	v_lshlrev_b32_e32 v57, 8, v57
	v_and_b32_e32 v67, 0xffff0000, v67
	v_and_b32_e32 v57, 0xff00, v57
	v_and_b32_e32 v59, 0xff0000, v59
	v_perm_b32 v55, v64, v55, s7
	v_mul_f32_e32 v65, v53, v65
	v_and_b32_e32 v68, 0xff0000, v66
	v_or3_b32 v66, v55, v57, v59
	v_mul_f32_e32 v55, v53, v67
	v_rndne_f32_e32 v65, v65
	v_rndne_f32_e32 v55, v55
	v_cvt_i32_f32_e32 v65, v65
	v_cvt_i32_f32_e32 v55, v55
	s_waitcnt vmcnt(8)
	v_lshlrev_b32_e32 v57, 16, v39
	v_and_b32_e32 v39, 0xffff0000, v39
	v_mul_f32_e32 v57, v53, v57
	v_perm_b32 v55, v55, v65, s7
	v_or3_b32 v67, v55, v69, v68
	v_lshlrev_b32_e32 v55, 16, v38
	v_and_b32_e32 v38, 0xffff0000, v38
	v_mul_f32_e32 v38, v53, v38
	v_mul_f32_e32 v55, v53, v55
	v_rndne_f32_e32 v38, v38
	v_mul_f32_e32 v39, v53, v39
	v_rndne_f32_e32 v55, v55
	v_cvt_i32_f32_e32 v38, v38
	v_rndne_f32_e32 v57, v57
	v_rndne_f32_e32 v39, v39
	v_cvt_i32_f32_e32 v55, v55
	v_cvt_i32_f32_sdwa v57, v57 dst_sel:WORD_1 dst_unused:UNUSED_PAD src0_sel:DWORD
	v_cvt_i32_f32_e32 v39, v39
	v_lshl_add_u64 v[64:65], v[62:63], 0, v[44:45]
	v_lshlrev_b32_e32 v59, 16, v40
	v_and_b32_e32 v40, 0xffff0000, v40
	v_lshlrev_b32_e32 v38, 8, v38
	global_load_dwordx4 v[2:5], v[2:3], off sc1
	v_and_b32_e32 v38, 0xff00, v38
	global_store_dwordx2 v[64:65], v[66:67], off
	v_lshlrev_b32_e32 v66, 16, v41
	v_and_b32_e32 v41, 0xffff0000, v41
	v_mul_f32_e32 v40, v53, v40
	v_and_b32_e32 v57, 0xff0000, v57
	v_perm_b32 v39, v39, v55, s7
	v_mul_f32_e32 v59, v53, v59
	v_rndne_f32_e32 v40, v40
	v_mul_f32_e32 v66, v53, v66
	v_or3_b32 v38, v39, v38, v57
	v_mul_f32_e32 v39, v53, v41
	v_rndne_f32_e32 v59, v59
	v_cvt_i32_f32_e32 v40, v40
	v_rndne_f32_e32 v66, v66
	v_rndne_f32_e32 v39, v39
	v_cvt_i32_f32_e32 v59, v59
	v_cvt_i32_f32_sdwa v66, v66 dst_sel:WORD_1 dst_unused:UNUSED_PAD src0_sel:DWORD
	v_cvt_i32_f32_e32 v39, v39
	v_lshlrev_b32_e32 v40, 8, v40
	v_and_b32_e32 v40, 0xff00, v40
	v_and_b32_e32 v66, 0xff0000, v66
	v_perm_b32 v39, v39, v59, s7
	v_or3_b32 v39, v39, v40, v66
	global_store_dwordx2 v[64:65], v[38:39], off offset:512
	s_waitcnt vmcnt(10)
	v_lshlrev_b32_e32 v38, 16, v34
	v_and_b32_e32 v34, 0xffff0000, v34
	v_lshlrev_b32_e32 v39, 16, v35
	v_and_b32_e32 v35, 0xffff0000, v35
	v_mul_f32_e32 v34, v53, v34
	v_mul_f32_e32 v38, v53, v38
	v_rndne_f32_e32 v34, v34
	v_mul_f32_e32 v39, v53, v39
	v_mul_f32_e32 v35, v53, v35
	v_rndne_f32_e32 v38, v38
	v_cvt_i32_f32_e32 v34, v34
	v_rndne_f32_e32 v39, v39
	v_rndne_f32_e32 v35, v35
	v_cvt_i32_f32_e32 v38, v38
	v_cvt_i32_f32_sdwa v39, v39 dst_sel:WORD_1 dst_unused:UNUSED_PAD src0_sel:DWORD
	v_cvt_i32_f32_e32 v35, v35
	v_lshlrev_b32_e32 v40, 16, v36
	v_and_b32_e32 v36, 0xffff0000, v36
	v_lshlrev_b32_e32 v34, 8, v34
	v_lshlrev_b32_e32 v41, 16, v37
	v_and_b32_e32 v37, 0xffff0000, v37
	v_and_b32_e32 v34, 0xff00, v34
	v_mul_f32_e32 v36, v53, v36
	v_and_b32_e32 v39, 0xff0000, v39
	v_perm_b32 v35, v35, v38, s7
	v_mul_f32_e32 v40, v53, v40
	v_rndne_f32_e32 v36, v36
	v_mul_f32_e32 v41, v53, v41
	v_or3_b32 v34, v35, v34, v39
	v_mul_f32_e32 v35, v53, v37
	v_rndne_f32_e32 v40, v40
	v_cvt_i32_f32_e32 v36, v36
	v_rndne_f32_e32 v41, v41
	v_rndne_f32_e32 v35, v35
	v_cvt_i32_f32_e32 v40, v40
	v_cvt_i32_f32_sdwa v41, v41 dst_sel:WORD_1 dst_unused:UNUSED_PAD src0_sel:DWORD
	v_cvt_i32_f32_e32 v35, v35
	v_lshlrev_b32_e32 v36, 8, v36
	v_and_b32_e32 v36, 0xff00, v36
	v_and_b32_e32 v41, 0xff0000, v41
	v_perm_b32 v35, v35, v40, s7
	v_or3_b32 v35, v35, v36, v41
	global_store_dwordx2 v[64:65], v[34:35], off offset:1024
	s_waitcnt vmcnt(10)
	v_lshlrev_b32_e32 v34, 16, v30
	v_and_b32_e32 v30, 0xffff0000, v30
	v_lshlrev_b32_e32 v35, 16, v31
	v_and_b32_e32 v31, 0xffff0000, v31
	v_mul_f32_e32 v30, v53, v30
	v_mul_f32_e32 v34, v53, v34
	v_rndne_f32_e32 v30, v30
	v_mul_f32_e32 v35, v53, v35
	v_mul_f32_e32 v31, v53, v31
	v_rndne_f32_e32 v34, v34
	v_cvt_i32_f32_e32 v30, v30
	v_rndne_f32_e32 v35, v35
	v_rndne_f32_e32 v31, v31
	v_cvt_i32_f32_e32 v34, v34
	v_cvt_i32_f32_sdwa v35, v35 dst_sel:WORD_1 dst_unused:UNUSED_PAD src0_sel:DWORD
	v_cvt_i32_f32_e32 v31, v31
	v_lshlrev_b32_e32 v36, 16, v32
	v_and_b32_e32 v32, 0xffff0000, v32
	v_lshlrev_b32_e32 v30, 8, v30
	v_lshlrev_b32_e32 v37, 16, v33
	v_and_b32_e32 v33, 0xffff0000, v33
	v_and_b32_e32 v30, 0xff00, v30
	v_mul_f32_e32 v32, v53, v32
	v_and_b32_e32 v35, 0xff0000, v35
	v_perm_b32 v31, v31, v34, s7
	v_mul_f32_e32 v36, v53, v36
	v_rndne_f32_e32 v32, v32
	v_mul_f32_e32 v37, v53, v37
	v_or3_b32 v30, v31, v30, v35
	v_mul_f32_e32 v31, v53, v33
	v_rndne_f32_e32 v36, v36
	v_cvt_i32_f32_e32 v32, v32
	v_rndne_f32_e32 v37, v37
	v_rndne_f32_e32 v31, v31
	v_cvt_i32_f32_e32 v36, v36
	v_cvt_i32_f32_sdwa v37, v37 dst_sel:WORD_1 dst_unused:UNUSED_PAD src0_sel:DWORD
	v_cvt_i32_f32_e32 v31, v31
	v_lshlrev_b32_e32 v32, 8, v32
	v_and_b32_e32 v32, 0xff00, v32
	v_and_b32_e32 v37, 0xff0000, v37
	v_perm_b32 v31, v31, v36, s7
	v_or3_b32 v31, v31, v32, v37
	global_store_dwordx2 v[64:65], v[30:31], off offset:1536
	s_waitcnt vmcnt(10)
	v_lshlrev_b32_e32 v30, 16, v26
	v_and_b32_e32 v26, 0xffff0000, v26
	v_lshlrev_b32_e32 v31, 16, v27
	v_and_b32_e32 v27, 0xffff0000, v27
	v_mul_f32_e32 v26, v53, v26
	v_mul_f32_e32 v30, v53, v30
	v_rndne_f32_e32 v26, v26
	v_mul_f32_e32 v31, v53, v31
	v_mul_f32_e32 v27, v53, v27
	v_rndne_f32_e32 v30, v30
	v_cvt_i32_f32_e32 v26, v26
	v_rndne_f32_e32 v31, v31
	v_rndne_f32_e32 v27, v27
	v_cvt_i32_f32_e32 v30, v30
	v_cvt_i32_f32_sdwa v31, v31 dst_sel:WORD_1 dst_unused:UNUSED_PAD src0_sel:DWORD
	v_cvt_i32_f32_e32 v27, v27
	v_lshlrev_b32_e32 v32, 16, v28
	v_and_b32_e32 v28, 0xffff0000, v28
	v_lshlrev_b32_e32 v26, 8, v26
	v_lshlrev_b32_e32 v33, 16, v29
	v_and_b32_e32 v29, 0xffff0000, v29
	v_and_b32_e32 v26, 0xff00, v26
	v_mul_f32_e32 v28, v53, v28
	v_and_b32_e32 v31, 0xff0000, v31
	v_perm_b32 v27, v27, v30, s7
	v_mul_f32_e32 v32, v53, v32
	v_rndne_f32_e32 v28, v28
	v_mul_f32_e32 v33, v53, v33
	v_or3_b32 v26, v27, v26, v31
	v_mul_f32_e32 v27, v53, v29
	v_rndne_f32_e32 v32, v32
	v_cvt_i32_f32_e32 v28, v28
	v_rndne_f32_e32 v33, v33
	v_rndne_f32_e32 v27, v27
	v_cvt_i32_f32_e32 v32, v32
	v_cvt_i32_f32_sdwa v33, v33 dst_sel:WORD_1 dst_unused:UNUSED_PAD src0_sel:DWORD
	v_cvt_i32_f32_e32 v27, v27
	v_lshlrev_b32_e32 v28, 8, v28
	v_and_b32_e32 v28, 0xff00, v28
	v_and_b32_e32 v33, 0xff0000, v33
	v_perm_b32 v27, v27, v32, s7
	v_or3_b32 v27, v27, v28, v33
	global_store_dwordx2 v[64:65], v[26:27], off offset:2048
	s_waitcnt vmcnt(10)
	v_lshlrev_b32_e32 v26, 16, v22
	v_and_b32_e32 v22, 0xffff0000, v22
	v_lshlrev_b32_e32 v27, 16, v23
	v_and_b32_e32 v23, 0xffff0000, v23
	v_mul_f32_e32 v22, v53, v22
	v_mul_f32_e32 v26, v53, v26
	v_rndne_f32_e32 v22, v22
	v_mul_f32_e32 v27, v53, v27
	v_mul_f32_e32 v23, v53, v23
	v_rndne_f32_e32 v26, v26
	v_cvt_i32_f32_e32 v22, v22
	v_rndne_f32_e32 v27, v27
	v_rndne_f32_e32 v23, v23
	v_cvt_i32_f32_e32 v26, v26
	v_cvt_i32_f32_sdwa v27, v27 dst_sel:WORD_1 dst_unused:UNUSED_PAD src0_sel:DWORD
	v_cvt_i32_f32_e32 v23, v23
	v_lshlrev_b32_e32 v28, 16, v24
	v_and_b32_e32 v24, 0xffff0000, v24
	v_lshlrev_b32_e32 v22, 8, v22
	v_lshlrev_b32_e32 v29, 16, v25
	v_and_b32_e32 v25, 0xffff0000, v25
	v_and_b32_e32 v22, 0xff00, v22
	v_mul_f32_e32 v24, v53, v24
	v_and_b32_e32 v27, 0xff0000, v27
	v_perm_b32 v23, v23, v26, s7
	v_mul_f32_e32 v28, v53, v28
	v_rndne_f32_e32 v24, v24
	v_mul_f32_e32 v29, v53, v29
	v_or3_b32 v22, v23, v22, v27
	v_mul_f32_e32 v23, v53, v25
	v_rndne_f32_e32 v28, v28
	v_cvt_i32_f32_e32 v24, v24
	v_rndne_f32_e32 v29, v29
	v_rndne_f32_e32 v23, v23
	v_cvt_i32_f32_e32 v28, v28
	v_cvt_i32_f32_sdwa v29, v29 dst_sel:WORD_1 dst_unused:UNUSED_PAD src0_sel:DWORD
	v_cvt_i32_f32_e32 v23, v23
	v_lshlrev_b32_e32 v24, 8, v24
	v_and_b32_e32 v24, 0xff00, v24
	v_and_b32_e32 v29, 0xff0000, v29
	v_perm_b32 v23, v23, v28, s7
	v_or3_b32 v23, v23, v24, v29
	global_store_dwordx2 v[64:65], v[22:23], off offset:2560
	s_waitcnt vmcnt(10)
	v_lshlrev_b32_e32 v22, 16, v18
	v_and_b32_e32 v18, 0xffff0000, v18
	v_lshlrev_b32_e32 v23, 16, v19
	v_and_b32_e32 v19, 0xffff0000, v19
	v_mul_f32_e32 v18, v53, v18
	v_mul_f32_e32 v22, v53, v22
	v_rndne_f32_e32 v18, v18
	v_mul_f32_e32 v23, v53, v23
	v_mul_f32_e32 v19, v53, v19
	v_rndne_f32_e32 v22, v22
	v_cvt_i32_f32_e32 v18, v18
	v_rndne_f32_e32 v23, v23
	v_rndne_f32_e32 v19, v19
	v_cvt_i32_f32_e32 v22, v22
	v_cvt_i32_f32_sdwa v23, v23 dst_sel:WORD_1 dst_unused:UNUSED_PAD src0_sel:DWORD
	v_cvt_i32_f32_e32 v19, v19
	v_lshlrev_b32_e32 v24, 16, v20
	v_and_b32_e32 v20, 0xffff0000, v20
	v_lshlrev_b32_e32 v18, 8, v18
	v_lshlrev_b32_e32 v25, 16, v21
	v_and_b32_e32 v21, 0xffff0000, v21
	v_and_b32_e32 v18, 0xff00, v18
	v_mul_f32_e32 v20, v53, v20
	v_and_b32_e32 v23, 0xff0000, v23
	v_perm_b32 v19, v19, v22, s7
	v_mul_f32_e32 v24, v53, v24
	v_rndne_f32_e32 v20, v20
	v_mul_f32_e32 v25, v53, v25
	v_or3_b32 v18, v19, v18, v23
	v_mul_f32_e32 v19, v53, v21
	v_rndne_f32_e32 v24, v24
	v_cvt_i32_f32_e32 v20, v20
	v_rndne_f32_e32 v25, v25
	v_rndne_f32_e32 v19, v19
	v_cvt_i32_f32_e32 v24, v24
	v_cvt_i32_f32_sdwa v25, v25 dst_sel:WORD_1 dst_unused:UNUSED_PAD src0_sel:DWORD
	v_cvt_i32_f32_e32 v19, v19
	v_lshlrev_b32_e32 v20, 8, v20
	v_and_b32_e32 v20, 0xff00, v20
	v_and_b32_e32 v25, 0xff0000, v25
	v_perm_b32 v19, v19, v24, s7
	v_or3_b32 v19, v19, v20, v25
	global_store_dwordx2 v[64:65], v[18:19], off offset:3072
	s_waitcnt vmcnt(10)
	v_lshlrev_b32_e32 v18, 16, v14
	v_and_b32_e32 v14, 0xffff0000, v14
	v_lshlrev_b32_e32 v19, 16, v15
	v_and_b32_e32 v15, 0xffff0000, v15
	v_mul_f32_e32 v14, v53, v14
	v_mul_f32_e32 v18, v53, v18
	v_rndne_f32_e32 v14, v14
	v_mul_f32_e32 v19, v53, v19
	v_mul_f32_e32 v15, v53, v15
	v_rndne_f32_e32 v18, v18
	v_cvt_i32_f32_e32 v14, v14
	v_rndne_f32_e32 v19, v19
	v_rndne_f32_e32 v15, v15
	v_cvt_i32_f32_e32 v18, v18
	v_cvt_i32_f32_sdwa v19, v19 dst_sel:WORD_1 dst_unused:UNUSED_PAD src0_sel:DWORD
	v_cvt_i32_f32_e32 v15, v15
	v_lshlrev_b32_e32 v20, 16, v16
	v_and_b32_e32 v16, 0xffff0000, v16
	v_lshlrev_b32_e32 v14, 8, v14
	v_lshlrev_b32_e32 v21, 16, v17
	v_and_b32_e32 v17, 0xffff0000, v17
	v_and_b32_e32 v14, 0xff00, v14
	v_mul_f32_e32 v16, v53, v16
	v_and_b32_e32 v19, 0xff0000, v19
	v_perm_b32 v15, v15, v18, s7
	v_mul_f32_e32 v20, v53, v20
	v_rndne_f32_e32 v16, v16
	v_mul_f32_e32 v21, v53, v21
	v_or3_b32 v14, v15, v14, v19
	v_mul_f32_e32 v15, v53, v17
	v_rndne_f32_e32 v20, v20
	v_cvt_i32_f32_e32 v16, v16
	v_rndne_f32_e32 v21, v21
	v_rndne_f32_e32 v15, v15
	v_cvt_i32_f32_e32 v20, v20
	v_cvt_i32_f32_sdwa v21, v21 dst_sel:WORD_1 dst_unused:UNUSED_PAD src0_sel:DWORD
	v_cvt_i32_f32_e32 v15, v15
	v_lshlrev_b32_e32 v16, 8, v16
	v_and_b32_e32 v16, 0xff00, v16
	v_and_b32_e32 v21, 0xff0000, v21
	v_perm_b32 v15, v15, v20, s7
	v_or3_b32 v15, v15, v16, v21
	global_store_dwordx2 v[64:65], v[14:15], off offset:3584
	s_waitcnt vmcnt(10)
	v_lshlrev_b32_e32 v14, 16, v10
	v_and_b32_e32 v10, 0xffff0000, v10
	v_lshlrev_b32_e32 v15, 16, v11
	v_and_b32_e32 v11, 0xffff0000, v11
	v_mul_f32_e32 v10, v53, v10
	v_mul_f32_e32 v14, v53, v14
	v_rndne_f32_e32 v10, v10
	v_mul_f32_e32 v15, v53, v15
	v_mul_f32_e32 v11, v53, v11
	v_rndne_f32_e32 v14, v14
	v_cvt_i32_f32_e32 v10, v10
	v_rndne_f32_e32 v15, v15
	v_rndne_f32_e32 v11, v11
	v_cvt_i32_f32_e32 v14, v14
	v_cvt_i32_f32_sdwa v15, v15 dst_sel:WORD_1 dst_unused:UNUSED_PAD src0_sel:DWORD
	v_cvt_i32_f32_e32 v11, v11
	v_lshlrev_b32_e32 v16, 16, v12
	v_and_b32_e32 v12, 0xffff0000, v12
	v_lshlrev_b32_e32 v10, 8, v10
	v_lshlrev_b32_e32 v17, 16, v13
	v_and_b32_e32 v13, 0xffff0000, v13
	v_and_b32_e32 v10, 0xff00, v10
	v_mul_f32_e32 v12, v53, v12
	v_and_b32_e32 v15, 0xff0000, v15
	v_perm_b32 v11, v11, v14, s7
	v_mul_f32_e32 v16, v53, v16
	v_rndne_f32_e32 v12, v12
	v_mul_f32_e32 v17, v53, v17
	v_or3_b32 v10, v11, v10, v15
	v_mul_f32_e32 v11, v53, v13
	v_rndne_f32_e32 v16, v16
	v_cvt_i32_f32_e32 v12, v12
	v_rndne_f32_e32 v17, v17
	v_rndne_f32_e32 v11, v11
	v_cvt_i32_f32_e32 v16, v16
	v_cvt_i32_f32_sdwa v17, v17 dst_sel:WORD_1 dst_unused:UNUSED_PAD src0_sel:DWORD
	v_cvt_i32_f32_e32 v11, v11
	v_lshlrev_b32_e32 v12, 8, v12
	v_and_b32_e32 v12, 0xff00, v12
	v_and_b32_e32 v17, 0xff0000, v17
	v_perm_b32 v11, v11, v16, s7
	v_or3_b32 v11, v11, v12, v17
	v_lshl_add_u64 v[12:13], v[62:63], 0, v[46:47]
	global_store_dwordx2 v[12:13], v[10:11], off
	s_waitcnt vmcnt(10)
	v_lshlrev_b32_e32 v10, 16, v6
	v_and_b32_e32 v6, 0xffff0000, v6
	v_lshlrev_b32_e32 v11, 16, v7
	v_and_b32_e32 v7, 0xffff0000, v7
	v_mul_f32_e32 v6, v53, v6
	v_mul_f32_e32 v10, v53, v10
	v_rndne_f32_e32 v6, v6
	v_mul_f32_e32 v11, v53, v11
	v_mul_f32_e32 v7, v53, v7
	v_rndne_f32_e32 v10, v10
	v_cvt_i32_f32_e32 v6, v6
	v_rndne_f32_e32 v11, v11
	v_rndne_f32_e32 v7, v7
	v_cvt_i32_f32_e32 v10, v10
	v_cvt_i32_f32_sdwa v11, v11 dst_sel:WORD_1 dst_unused:UNUSED_PAD src0_sel:DWORD
	v_cvt_i32_f32_e32 v7, v7
	v_lshlrev_b32_e32 v12, 16, v8
	v_and_b32_e32 v8, 0xffff0000, v8
	v_lshlrev_b32_e32 v6, 8, v6
	v_lshlrev_b32_e32 v13, 16, v9
	v_and_b32_e32 v9, 0xffff0000, v9
	v_and_b32_e32 v6, 0xff00, v6
	v_mul_f32_e32 v8, v53, v8
	v_and_b32_e32 v11, 0xff0000, v11
	v_perm_b32 v7, v7, v10, s7
	v_mul_f32_e32 v12, v53, v12
	v_rndne_f32_e32 v8, v8
	v_mul_f32_e32 v13, v53, v13
	v_or3_b32 v6, v7, v6, v11
	v_mul_f32_e32 v7, v53, v9
	v_rndne_f32_e32 v12, v12
	v_cvt_i32_f32_e32 v8, v8
	v_rndne_f32_e32 v13, v13
	v_rndne_f32_e32 v7, v7
	v_cvt_i32_f32_e32 v12, v12
	v_cvt_i32_f32_sdwa v13, v13 dst_sel:WORD_1 dst_unused:UNUSED_PAD src0_sel:DWORD
	v_cvt_i32_f32_e32 v7, v7
	v_lshlrev_b32_e32 v8, 8, v8
	v_and_b32_e32 v8, 0xff00, v8
	v_and_b32_e32 v13, 0xff0000, v13
	v_perm_b32 v7, v7, v12, s7
	v_or3_b32 v7, v7, v8, v13
	v_lshl_add_u64 v[8:9], v[62:63], 0, v[48:49]
	global_store_dwordx2 v[8:9], v[6:7], off
	s_waitcnt vmcnt(10)
	v_lshlrev_b32_e32 v6, 16, v2
	v_and_b32_e32 v2, 0xffff0000, v2
	v_lshlrev_b32_e32 v7, 16, v3
	v_and_b32_e32 v3, 0xffff0000, v3
	v_mul_f32_e32 v2, v53, v2
	v_mul_f32_e32 v6, v53, v6
	v_rndne_f32_e32 v2, v2
	v_mul_f32_e32 v7, v53, v7
	v_mul_f32_e32 v3, v53, v3
	v_rndne_f32_e32 v6, v6
	v_cvt_i32_f32_e32 v2, v2
	v_rndne_f32_e32 v7, v7
	v_rndne_f32_e32 v3, v3
	v_cvt_i32_f32_e32 v6, v6
	v_cvt_i32_f32_sdwa v7, v7 dst_sel:WORD_1 dst_unused:UNUSED_PAD src0_sel:DWORD
	v_cvt_i32_f32_e32 v3, v3
	v_lshlrev_b32_e32 v8, 16, v4
	v_and_b32_e32 v4, 0xffff0000, v4
	v_lshlrev_b32_e32 v2, 8, v2
	v_lshlrev_b32_e32 v9, 16, v5
	v_and_b32_e32 v5, 0xffff0000, v5
	v_and_b32_e32 v2, 0xff00, v2
	v_mul_f32_e32 v4, v53, v4
	v_and_b32_e32 v7, 0xff0000, v7
	v_perm_b32 v3, v3, v6, s7
	v_mul_f32_e32 v8, v53, v8
	v_rndne_f32_e32 v4, v4
	v_mul_f32_e32 v9, v53, v9
	v_or3_b32 v2, v3, v2, v7
	v_mul_f32_e32 v3, v53, v5
	v_rndne_f32_e32 v8, v8
	v_cvt_i32_f32_e32 v4, v4
	v_rndne_f32_e32 v9, v9
	v_rndne_f32_e32 v3, v3
	v_cvt_i32_f32_e32 v8, v8
	v_cvt_i32_f32_sdwa v9, v9 dst_sel:WORD_1 dst_unused:UNUSED_PAD src0_sel:DWORD
	v_cvt_i32_f32_e32 v3, v3
	v_lshlrev_b32_e32 v4, 8, v4
	v_and_b32_e32 v4, 0xff00, v4
	v_and_b32_e32 v9, 0xff0000, v9
	v_perm_b32 v3, v3, v8, s7
	v_or3_b32 v3, v3, v4, v9
	v_lshl_add_u64 v[4:5], v[62:63], 0, v[50:51]
	global_store_dwordx2 v[4:5], v[2:3], off
	s_and_saveexec_b64 s[4:5], s[0:1]
	s_cbranch_execz .LBB0_1944
	v_mul_f32_e32 v2, 0x3c010204, v43
	global_store_dword v[60:61], v2, off
	s_branch .LBB0_1944

.LBB0_2067:
	s_or_b64 exec, exec, s[0:1]
	v_mov_b32_e32 v4, v0
	s_waitcnt lgkmcnt(0)
	s_barrier
	v_readlane_b32 s0, v255, 28
	v_ashrrev_i32_e32 v1, 6, v4
	s_nop 0
	v_add_u32_e32 v34, s0, v1
	s_movk_i32 s0, 0x4000
	v_cmp_gt_i32_e32 vcc, s0, v34
	s_and_saveexec_b64 s[22:23], vcc
	s_cbranch_execz .LBB0_2072
	v_lshlrev_b32_e32 v2, 1, v34
	v_ashrrev_i32_e32 v3, 31, v2
	v_readlane_b32 s0, v253, 41
	v_lshlrev_b64 v[2:3], 2, v[2:3]
	v_readlane_b32 s1, v253, 42
	v_lshlrev_b32_e32 v4, 2, v4
	v_and_b32_e32 v18, 0xfc, v4
	v_lshl_add_u64 v[6:7], s[0:1], 0, v[2:3]
	v_lshl_add_u64 v[2:3], s[18:19], 0, v[2:3]
	global_load_dwordx2 v[78:79], v[6:7], off sc1
	s_nop 0
	global_load_dwordx2 v[2:3], v[2:3], off sc1
	v_readlane_b32 s0, v255, 29
	v_lshlrev_b32_e32 v98, 2, v18
	v_or_b32_e32 v20, 0x400, v18
	v_add_lshl_u32 v30, s0, v1, 1
	v_or_b32_e32 v22, 0x500, v18
	v_or_b32_e32 v24, 0x600, v18
	v_or_b32_e32 v26, 0x700, v18
	v_readlane_b32 s0, v254, 24
	v_readlane_b32 s36, v251, 1
	v_mov_b32_e32 v5, v99
	v_mov_b32_e32 v7, v99
	v_mov_b32_e32 v9, v99
	v_mov_b32_e32 v11, v99
	v_mov_b32_e32 v13, v99
	v_mov_b32_e32 v15, v99
	v_mov_b32_e32 v17, v99
	v_readlane_b32 s1, v254, 25
	v_or_b32_e32 v4, 0x400, v98
	v_or_b32_e32 v6, 0x800, v98
	v_or_b32_e32 v8, 0xc00, v98
	v_lshlrev_b32_e32 v10, 2, v20
	v_lshlrev_b32_e32 v12, 2, v22
	v_lshlrev_b32_e32 v14, 2, v24
	v_lshlrev_b32_e32 v16, 2, v26
	v_readlane_b32 s42, v251, 7
	v_readlane_b32 s43, v251, 8
	v_lshl_add_u64 v[32:33], s[0:1], 0, v[98:99]
	s_mov_b64 s[18:19], s[42:43]
	v_lshl_add_u64 v[46:47], s[0:1], 0, v[4:5]
	v_lshl_add_u64 v[48:49], s[0:1], 0, v[6:7]
	v_lshl_add_u64 v[50:51], s[0:1], 0, v[8:9]
	v_lshl_add_u64 v[52:53], s[0:1], 0, v[10:11]
	v_lshl_add_u64 v[54:55], s[0:1], 0, v[12:13]
	v_lshl_add_u64 v[56:57], s[0:1], 0, v[14:15]
	v_lshl_add_u64 v[58:59], s[0:1], 0, v[16:17]
	v_readlane_b32 s0, v252, 15
	v_lshl_add_u64 v[36:37], s[18:19], 0, v[98:99]
	v_lshlrev_b32_e32 v98, 1, v18
	v_readlane_b32 s4, v253, 50
	v_readlane_b32 s1, v252, 16
	s_mov_b64 s[24:25], 0
	v_lshlrev_b32_e32 v38, 2, v20
	v_lshlrev_b32_e32 v40, 2, v22
	v_lshlrev_b32_e32 v42, 2, v24
	v_lshlrev_b32_e32 v44, 2, v26
	v_lshl_add_u64 v[60:61], s[18:19], 0, v[10:11]
	v_lshl_add_u64 v[62:63], s[18:19], 0, v[12:13]
	v_lshl_add_u64 v[64:65], s[18:19], 0, v[14:15]
	v_lshl_add_u64 v[66:67], s[18:19], 0, v[16:17]
	v_readlane_b32 s5, v253, 51
	v_lshl_add_u64 v[68:69], s[0:1], 0, v[98:99]
	v_lshlrev_b32_e32 v98, 2, v18
	v_readlane_b32 s37, v251, 2
	v_readlane_b32 s38, v251, 3
	v_readlane_b32 s39, v251, 4
	v_readlane_b32 s40, v251, 5
	v_readlane_b32 s41, v251, 6
	s_waitcnt vmcnt(1)
	v_mov_b64_e32 v[70:71], v[78:79]
	s_waitcnt vmcnt(0)
	v_mov_b64_e32 v[72:73], v[2:3]
	s_branch .LBB0_2070
.LBB0_2069:
	s_or_b64 exec, exec, s[26:27]
	v_ashrrev_i32_e32 v7, 31, v2
	v_mov_b32_e32 v6, v2
	v_ashrrev_i32_e32 v9, 31, v3
	v_mov_b32_e32 v8, v3
	v_lshlrev_b64 v[6:7], 12, v[6:7]
	v_lshlrev_b64 v[2:3], 12, v[8:9]
	v_lshl_add_u64 v[74:75], v[68:69], 0, v[6:7]
	v_lshl_add_u64 v[2:3], v[68:69], 0, v[2:3]
	global_load_dwordx2 v[76:77], v[74:75], off sc1
	global_load_dwordx2 v[110:111], v[2:3], off sc1
	v_add_u32_e32 v4, 0x100, v34
	v_ashrrev_i32_e32 v5, 31, v4
	v_lshlrev_b64 v[4:5], 13, v[4:5]
	v_lshl_add_u64 v[4:5], s[76:77], 0, v[4:5]
	v_lshl_add_u64 v[6:7], v[4:5], 0, v[98:99]
	v_mov_b32_e32 v39, v99
	global_load_dwordx4 v[106:109], v[6:7], off sc1
	global_load_dwordx2 v[114:115], v[74:75], off offset:512 sc1
	global_load_dwordx2 v[116:117], v[2:3], off offset:512 sc1
	global_load_dwordx4 v[26:29], v[6:7], off offset:1024 sc1
	global_load_dwordx2 v[104:105], v[74:75], off offset:1024 sc1
	global_load_dwordx2 v[102:103], v[2:3], off offset:1024 sc1
	global_load_dwordx4 v[22:25], v[6:7], off offset:2048 sc1
	global_load_dwordx2 v[100:101], v[74:75], off offset:1536 sc1
	global_load_dwordx2 v[96:97], v[2:3], off offset:1536 sc1
	global_load_dwordx4 v[18:21], v[6:7], off offset:3072 sc1
	global_load_dwordx2 v[94:95], v[74:75], off offset:2048 sc1
	global_load_dwordx2 v[92:93], v[2:3], off offset:2048 sc1
	v_lshl_add_u64 v[6:7], v[4:5], 0, v[38:39]
	v_mov_b32_e32 v41, v99
	global_load_dwordx4 v[14:17], v[6:7], off sc1
	global_load_dwordx2 v[90:91], v[74:75], off offset:2560 sc1
	global_load_dwordx2 v[88:89], v[2:3], off offset:2560 sc1
	v_lshl_add_u64 v[6:7], v[4:5], 0, v[40:41]
	v_mov_b32_e32 v43, v99
	global_load_dwordx4 v[10:13], v[6:7], off sc1
	global_load_dwordx2 v[86:87], v[74:75], off offset:3072 sc1
	global_load_dwordx2 v[84:85], v[2:3], off offset:3072 sc1
	v_lshl_add_u64 v[6:7], v[4:5], 0, v[42:43]
	v_mov_b32_e32 v45, v99
	global_load_dwordx4 v[6:9], v[6:7], off sc1
	s_nop 0
	global_load_dwordx2 v[82:83], v[74:75], off offset:3584 sc1
	global_load_dwordx2 v[80:81], v[2:3], off offset:3584 sc1
	v_lshl_add_u64 v[2:3], v[4:5], 0, v[44:45]
	global_load_dwordx4 v[2:5], v[2:3], off sc1
	s_and_b64 s[0:1], exec, vcc
	s_or_b64 s[24:25], s[0:1], s[24:25]
	s_mov_b32 s0, 0x800000
	s_waitcnt vmcnt(23)
	v_lshlrev_b32_e32 v74, 16, v76
	s_waitcnt vmcnt(22)
	v_lshlrev_b32_e32 v112, 16, v110
	v_and_b32_e32 v113, 0xffff0000, v110
	v_lshlrev_b32_e32 v110, 16, v111
	v_and_b32_e32 v111, 0xffff0000, v111
	v_and_b32_e32 v75, 0xffff0000, v76
	v_lshlrev_b32_e32 v76, 16, v77
	v_and_b32_e32 v77, 0xffff0000, v77
	v_pk_mul_f32 v[110:111], v[78:79], v[110:111] op_sel:[1,0]
	v_pk_mul_f32 v[112:113], v[78:79], v[112:113] op_sel:[1,0]
	s_nop 0
	v_pk_fma_f32 v[118:119], v[78:79], v[74:75], v[112:113] op_sel_hi:[0,1,1]
	v_pk_fma_f32 v[74:75], v[78:79], v[76:77], v[110:111] op_sel_hi:[0,1,1]
	global_load_dwordx4 v[110:113], v[32:33], off sc1
	s_waitcnt vmcnt(0)
	v_pk_fma_f32 v[74:75], v[74:75], v[112:113], v[108:109]
	v_pk_fma_f32 v[76:77], v[118:119], v[110:111], v[106:107]
	v_lshlrev_b32_e32 v110, 16, v116
	v_and_b32_e32 v111, 0xffff0000, v116
	v_lshlrev_b32_e32 v112, 16, v117
	v_and_b32_e32 v113, 0xffff0000, v117
	v_lshlrev_b32_e32 v106, 16, v114
	v_and_b32_e32 v107, 0xffff0000, v114
	v_lshlrev_b32_e32 v108, 16, v115
	v_and_b32_e32 v109, 0xffff0000, v115
	v_pk_mul_f32 v[112:113], v[78:79], v[112:113] op_sel:[1,0]
	v_pk_mul_f32 v[110:111], v[78:79], v[110:111] op_sel:[1,0]
	v_pk_fma_f32 v[112:113], v[78:79], v[108:109], v[112:113] op_sel_hi:[0,1,1]
	v_pk_fma_f32 v[110:111], v[78:79], v[106:107], v[110:111] op_sel_hi:[0,1,1]
	global_load_dwordx4 v[106:109], v[46:47], off sc1
	v_mul_f32_e32 v31, v77, v77
	v_fmac_f32_e32 v31, v76, v76
	v_fmac_f32_e32 v31, v74, v74
	v_fmac_f32_e32 v31, v75, v75
	s_waitcnt vmcnt(0)
	v_pk_fma_f32 v[28:29], v[112:113], v[108:109], v[28:29]
	v_lshlrev_b32_e32 v108, 16, v102
	v_and_b32_e32 v109, 0xffff0000, v102
	v_lshlrev_b32_e32 v102, 16, v103
	v_and_b32_e32 v103, 0xffff0000, v103
	v_pk_fma_f32 v[26:27], v[110:111], v[106:107], v[26:27]
	v_lshlrev_b32_e32 v106, 16, v104
	v_and_b32_e32 v107, 0xffff0000, v104
	v_lshlrev_b32_e32 v104, 16, v105
	v_and_b32_e32 v105, 0xffff0000, v105
	v_pk_mul_f32 v[102:103], v[78:79], v[102:103] op_sel:[1,0]
	v_pk_mul_f32 v[108:109], v[78:79], v[108:109] op_sel:[1,0]
	v_mul_f32_e32 v35, v27, v27
	v_pk_fma_f32 v[106:107], v[78:79], v[106:107], v[108:109] op_sel_hi:[0,1,1]
	v_pk_fma_f32 v[108:109], v[78:79], v[104:105], v[102:103] op_sel_hi:[0,1,1]
	global_load_dwordx4 v[102:105], v[48:49], off sc1
	v_fmac_f32_e32 v35, v26, v26
	v_fmac_f32_e32 v35, v28, v28
	v_fmac_f32_e32 v35, v29, v29
	v_add_f32_e32 v31, v31, v35
	s_waitcnt vmcnt(0)
	v_pk_fma_f32 v[24:25], v[108:109], v[104:105], v[24:25]
	v_lshlrev_b32_e32 v104, 16, v96
	v_and_b32_e32 v105, 0xffff0000, v96
	v_lshlrev_b32_e32 v96, 16, v97
	v_and_b32_e32 v97, 0xffff0000, v97
	v_pk_fma_f32 v[22:23], v[106:107], v[102:103], v[22:23]
	v_lshlrev_b32_e32 v102, 16, v100
	v_and_b32_e32 v103, 0xffff0000, v100
	v_lshlrev_b32_e32 v100, 16, v101
	v_and_b32_e32 v101, 0xffff0000, v101
	v_pk_mul_f32 v[96:97], v[78:79], v[96:97] op_sel:[1,0]
	v_pk_mul_f32 v[104:105], v[78:79], v[104:105] op_sel:[1,0]
	v_pk_fma_f32 v[96:97], v[78:79], v[100:101], v[96:97] op_sel_hi:[0,1,1]
	v_pk_fma_f32 v[104:105], v[78:79], v[102:103], v[104:105] op_sel_hi:[0,1,1]
	global_load_dwordx4 v[100:103], v[50:51], off sc1
	v_mul_f32_e32 v35, v23, v23
	v_fmac_f32_e32 v35, v22, v22
	v_fmac_f32_e32 v35, v24, v24
	v_fmac_f32_e32 v35, v25, v25
	v_add_f32_e32 v31, v31, v35
	s_waitcnt vmcnt(0)
	v_pk_fma_f32 v[18:19], v[104:105], v[100:101], v[18:19]
	v_lshlrev_b32_e32 v100, 16, v92
	v_and_b32_e32 v101, 0xffff0000, v92
	v_lshlrev_b32_e32 v92, 16, v93
	v_and_b32_e32 v93, 0xffff0000, v93
	v_pk_fma_f32 v[20:21], v[96:97], v[102:103], v[20:21]
	v_lshlrev_b32_e32 v96, 16, v94
	v_and_b32_e32 v97, 0xffff0000, v94
	v_lshlrev_b32_e32 v94, 16, v95
	v_and_b32_e32 v95, 0xffff0000, v95
	v_pk_mul_f32 v[92:93], v[78:79], v[92:93] op_sel:[1,0]
	v_pk_mul_f32 v[100:101], v[78:79], v[100:101] op_sel:[1,0]
	v_mul_f32_e32 v35, v19, v19
	v_pk_fma_f32 v[96:97], v[78:79], v[96:97], v[100:101] op_sel_hi:[0,1,1]
	v_pk_fma_f32 v[100:101], v[78:79], v[94:95], v[92:93] op_sel_hi:[0,1,1]
	global_load_dwordx4 v[92:95], v[52:53], off sc1
	v_fmac_f32_e32 v35, v18, v18
	v_fmac_f32_e32 v35, v20, v20
	v_fmac_f32_e32 v35, v21, v21
	v_add_f32_e32 v31, v31, v35
	v_mov_b32_e32 v35, v0
	s_waitcnt vmcnt(0)
	v_pk_fma_f32 v[16:17], v[100:101], v[94:95], v[16:17]
	v_lshlrev_b32_e32 v94, 16, v88
	v_and_b32_e32 v95, 0xffff0000, v88
	v_lshlrev_b32_e32 v88, 16, v89
	v_and_b32_e32 v89, 0xffff0000, v89
	v_pk_fma_f32 v[14:15], v[96:97], v[92:93], v[14:15]
	v_lshlrev_b32_e32 v92, 16, v90
	v_and_b32_e32 v93, 0xffff0000, v90
	v_lshlrev_b32_e32 v90, 16, v91
	v_and_b32_e32 v91, 0xffff0000, v91
	v_pk_mul_f32 v[88:89], v[78:79], v[88:89] op_sel:[1,0]
	v_pk_mul_f32 v[94:95], v[78:79], v[94:95] op_sel:[1,0]
	s_nop 0
	v_pk_fma_f32 v[92:93], v[78:79], v[92:93], v[94:95] op_sel_hi:[0,1,1]
	v_pk_fma_f32 v[94:95], v[78:79], v[90:91], v[88:89] op_sel_hi:[0,1,1]
	global_load_dwordx4 v[88:91], v[54:55], off sc1
	s_waitcnt vmcnt(0)
	v_pk_fma_f32 v[10:11], v[92:93], v[88:89], v[10:11]
	v_pk_fma_f32 v[12:13], v[94:95], v[90:91], v[12:13]
	v_mov_b32_e32 v90, v15
	v_mov_b32_e32 v91, v11
	v_mov_b32_e32 v88, v14
	v_mov_b32_e32 v89, v10
	v_pk_mul_f32 v[90:91], v[90:91], v[90:91]
	s_nop 0
	v_pk_fma_f32 v[88:89], v[88:89], v[88:89], v[90:91]
	v_mov_b32_e32 v90, v16
	v_mov_b32_e32 v91, v12
	v_pk_fma_f32 v[88:89], v[90:91], v[90:91], v[88:89]
	v_mov_b32_e32 v90, v17
	v_mov_b32_e32 v91, v13
	v_pk_fma_f32 v[88:89], v[90:91], v[90:91], v[88:89]
	v_lshlrev_b32_e32 v90, 16, v84
	v_add_f32_e32 v31, v31, v88
	v_and_b32_e32 v91, 0xffff0000, v84
	v_lshlrev_b32_e32 v84, 16, v85
	v_and_b32_e32 v85, 0xffff0000, v85
	v_add_f32_e32 v31, v31, v89
	v_lshlrev_b32_e32 v88, 16, v86
	v_and_b32_e32 v89, 0xffff0000, v86
	v_pk_mul_f32 v[92:93], v[78:79], v[84:85] op_sel:[1,0]
	v_pk_mul_f32 v[84:85], v[78:79], v[90:91] op_sel:[1,0]
	v_lshlrev_b32_e32 v86, 16, v87
	v_pk_fma_f32 v[84:85], v[78:79], v[88:89], v[84:85] op_sel_hi:[0,1,1]
	global_load_dwordx4 v[88:91], v[56:57], off sc1
	v_and_b32_e32 v87, 0xffff0000, v87
	v_pk_fma_f32 v[86:87], v[78:79], v[86:87], v[92:93] op_sel_hi:[0,1,1]
	s_waitcnt vmcnt(0)
	v_pk_fma_f32 v[8:9], v[86:87], v[90:91], v[8:9]
	v_lshlrev_b32_e32 v86, 16, v80
	v_and_b32_e32 v87, 0xffff0000, v80
	v_lshlrev_b32_e32 v80, 16, v81
	v_and_b32_e32 v81, 0xffff0000, v81
	v_pk_fma_f32 v[6:7], v[84:85], v[88:89], v[6:7]
	v_lshlrev_b32_e32 v84, 16, v82
	v_and_b32_e32 v85, 0xffff0000, v82
	v_lshlrev_b32_e32 v82, 16, v83
	v_and_b32_e32 v83, 0xffff0000, v83
	v_pk_mul_f32 v[80:81], v[78:79], v[80:81] op_sel:[1,0]
	v_pk_mul_f32 v[86:87], v[78:79], v[86:87] op_sel:[1,0]
	v_pk_fma_f32 v[82:83], v[78:79], v[82:83], v[80:81] op_sel_hi:[0,1,1]
	v_pk_fma_f32 v[84:85], v[78:79], v[84:85], v[86:87] op_sel_hi:[0,1,1]
	global_load_dwordx4 v[78:81], v[58:59], off sc1
	s_waitcnt vmcnt(0)
	v_pk_fma_f32 v[2:3], v[78:79], v[84:85], v[2:3]
	v_pk_fma_f32 v[4:5], v[80:81], v[82:83], v[4:5]
	v_mov_b32_e32 v80, v7
	v_mov_b32_e32 v81, v3
	v_mov_b32_e32 v78, v6
	v_mov_b32_e32 v79, v2
	v_pk_mul_f32 v[80:81], v[80:81], v[80:81]
	v_lshlrev_b32_e32 v35, 2, v35
	v_pk_fma_f32 v[78:79], v[78:79], v[78:79], v[80:81]
	v_mov_b32_e32 v80, v8
	v_mov_b32_e32 v81, v4
	v_pk_fma_f32 v[78:79], v[80:81], v[80:81], v[78:79]
	v_mov_b32_e32 v80, v9
	v_mov_b32_e32 v81, v5
	v_pk_fma_f32 v[78:79], v[80:81], v[80:81], v[78:79]
	s_nop 0
	v_add_f32_e32 v31, v31, v78
	v_add_f32_e32 v31, v31, v79
	v_bitop3_b32 v78, v35, s59, v220 bitop3:0x6c
	ds_bpermute_b32 v78, v78, v31
	s_waitcnt lgkmcnt(0)
	v_add_f32_e32 v31, v31, v78
	v_bitop3_b32 v78, v35, 64, v220 bitop3:0x6c
	ds_bpermute_b32 v78, v78, v31
	s_waitcnt lgkmcnt(0)
	v_add_f32_e32 v31, v31, v78
	v_bitop3_b32 v78, v35, 32, v220 bitop3:0x6c
	ds_bpermute_b32 v78, v78, v31
	s_waitcnt lgkmcnt(0)
	v_add_f32_e32 v31, v31, v78
	v_bitop3_b32 v78, v35, 16, v220 bitop3:0x6c
	ds_bpermute_b32 v78, v78, v31
	s_waitcnt lgkmcnt(0)
	v_add_f32_e32 v31, v31, v78
	v_bitop3_b32 v78, v35, 8, v220 bitop3:0x6c
	ds_bpermute_b32 v78, v78, v31
	v_bitop3_b32 v35, v35, 4, v220 bitop3:0x6c
	s_waitcnt lgkmcnt(0)
	v_add_f32_e32 v31, v31, v78
	global_load_dwordx4 v[78:81], v[36:37], off sc1
	global_load_dwordx4 v[82:85], v[36:37], off offset:1024 sc1
	global_load_dwordx4 v[86:89], v[36:37], off offset:2048 sc1
	global_load_dwordx4 v[90:93], v[36:37], off offset:3072 sc1
	global_load_dwordx4 v[94:97], v[60:61], off sc1
	global_load_dwordx4 v[100:103], v[62:63], off sc1
	global_load_dwordx4 v[104:107], v[64:65], off sc1
	global_load_dwordx4 v[108:111], v[66:67], off sc1
	ds_bpermute_b32 v35, v35, v31
	s_waitcnt lgkmcnt(0)
	v_add_f32_e32 v31, v31, v35
	v_fmamk_f32 v31, v31, 0x3a000000, v248
	v_cmp_gt_f32_e32 vcc, s0, v31
	v_mul_f32_e32 v35, 0x4b800000, v31
	v_readlane_b32 s0, v255, 27
	v_cndmask_b32_e32 v31, v31, v35, vcc
	v_rsq_f32_e32 v31, v31
	v_add_u32_e32 v30, s0, v30
	v_mul_f32_e32 v35, 0x45800000, v31
	v_cndmask_b32_e32 v112, v31, v35, vcc
	v_ashrrev_i32_e32 v35, 31, v34
	v_lshlrev_b64 v[34:35], 13, v[34:35]
	v_pk_mul_f32 v[114:115], v[76:77], v[112:113] op_sel_hi:[1,0]
	v_pk_mul_f32 v[74:75], v[74:75], v[112:113] op_sel_hi:[1,0]
	v_lshl_add_u64 v[34:35], s[12:13], 0, v[34:35]
	v_pk_mul_f32 v[18:19], v[18:19], v[112:113] op_sel_hi:[1,0]
	v_pk_mul_f32 v[20:21], v[20:21], v[112:113] op_sel_hi:[1,0]
	v_pk_mul_f32 v[14:15], v[14:15], v[112:113] op_sel_hi:[1,0]
	v_pk_mul_f32 v[16:17], v[16:17], v[112:113] op_sel_hi:[1,0]
	v_pk_mul_f32 v[10:11], v[10:11], v[112:113] op_sel_hi:[1,0]
	v_pk_mul_f32 v[12:13], v[12:13], v[112:113] op_sel_hi:[1,0]
	v_pk_mul_f32 v[6:7], v[6:7], v[112:113] op_sel_hi:[1,0]
	v_pk_mul_f32 v[8:9], v[8:9], v[112:113] op_sel_hi:[1,0]
	v_pk_mul_f32 v[26:27], v[26:27], v[112:113] op_sel_hi:[1,0]
	v_pk_mul_f32 v[28:29], v[28:29], v[112:113] op_sel_hi:[1,0]
	v_pk_mul_f32 v[22:23], v[22:23], v[112:113] op_sel_hi:[1,0]
	v_pk_mul_f32 v[24:25], v[24:25], v[112:113] op_sel_hi:[1,0]
	v_pk_mul_f32 v[2:3], v[2:3], v[112:113] op_sel_hi:[1,0]
	v_pk_mul_f32 v[4:5], v[4:5], v[112:113] op_sel_hi:[1,0]
	s_waitcnt vmcnt(7)
	v_pk_mul_f32 v[76:77], v[80:81], v[74:75]
	v_pk_mul_f32 v[74:75], v[78:79], v[114:115]
	v_lshl_add_u64 v[78:79], v[34:35], 0, v[98:99]
	s_waitcnt vmcnt(4)
	v_pk_mul_f32 v[20:21], v[92:93], v[20:21]
	v_pk_mul_f32 v[18:19], v[90:91], v[18:19]
	global_store_dwordx4 v[78:79], v[18:21], off offset:3072
	s_waitcnt vmcnt(4)
	v_pk_mul_f32 v[16:17], v[96:97], v[16:17]
	v_pk_mul_f32 v[14:15], v[94:95], v[14:15]
	v_lshl_add_u64 v[18:19], v[34:35], 0, v[38:39]
	global_store_dwordx4 v[18:19], v[14:17], off
	s_waitcnt vmcnt(4)
	v_pk_mul_f32 v[12:13], v[102:103], v[12:13]
	v_pk_mul_f32 v[10:11], v[100:101], v[10:11]
	v_lshl_add_u64 v[14:15], v[34:35], 0, v[40:41]
	global_store_dwordx4 v[14:15], v[10:13], off
	s_waitcnt vmcnt(4)
	v_pk_mul_f32 v[8:9], v[106:107], v[8:9]
	v_pk_mul_f32 v[6:7], v[104:105], v[6:7]
	v_lshl_add_u64 v[10:11], v[34:35], 0, v[42:43]
	v_pk_mul_f32 v[28:29], v[84:85], v[28:29]
	v_pk_mul_f32 v[26:27], v[82:83], v[26:27]
	v_pk_mul_f32 v[24:25], v[88:89], v[24:25]
	v_pk_mul_f32 v[22:23], v[86:87], v[22:23]
	global_store_dwordx4 v[10:11], v[6:9], off
	s_waitcnt vmcnt(4)
	v_pk_mul_f32 v[4:5], v[110:111], v[4:5]
	v_pk_mul_f32 v[2:3], v[108:109], v[2:3]
	v_lshl_add_u64 v[6:7], v[34:35], 0, v[44:45]
	global_store_dwordx4 v[78:79], v[74:77], off
	global_store_dwordx4 v[78:79], v[26:29], off offset:1024
	global_store_dwordx4 v[78:79], v[22:25], off offset:2048
	global_store_dwordx4 v[6:7], v[2:5], off
	v_mov_b32_e32 v34, v1
	v_mov_b64_e32 v[78:79], v[70:71]
	v_mov_b64_e32 v[2:3], v[72:73]
	s_andn2_b64 exec, exec, s[24:25]
	s_cbranch_execz .LBB0_2072
.LBB0_2070:
	v_add_u32_e32 v1, s33, v34
	s_movk_i32 s0, 0x4000
	s_movk_i32 s3, 0x3fff
	v_cmp_gt_i32_e64 s[0:1], s0, v1
	v_cmp_lt_i32_e32 vcc, s3, v1
	s_and_saveexec_b64 s[26:27], s[0:1]
	s_cbranch_execz .LBB0_2069
	v_ashrrev_i32_e32 v31, 31, v30
	v_lshlrev_b64 v[4:5], 2, v[30:31]
	v_add_u32_e32 v8, 1, v30
	v_readlane_b32 s0, v253, 41
	v_lshl_add_u64 v[6:7], s[4:5], 0, v[4:5]
	v_ashrrev_i32_e32 v9, 31, v8
	v_readlane_b32 s1, v253, 42
	s_nop 1
	v_lshl_add_u64 v[4:5], s[0:1], 0, v[4:5]
	v_lshl_add_u64 v[8:9], v[8:9], 2, s[0:1]
	global_load_dwordx2 v[72:73], v[6:7], off sc1
	global_load_dword v70, v[4:5], off sc1
	global_load_dword v71, v[8:9], off sc1
	s_branch .LBB0_2069

.LBB0_2163:
	v_readlane_b32 s4, v253, 57
	v_ashrrev_i32_e32 v43, 31, v42
	v_readlane_b32 s5, v253, 58
	s_movk_i32 s3, 0x2c00
	v_lshlrev_b32_e32 v98, 1, v44
	v_lshl_add_u64 v[60:61], v[42:43], 2, s[4:5]
	global_load_dword v1, v[60:61], off sc1
	v_readlane_b32 s4, v252, 59
	v_readlane_b32 s5, v252, 60
	v_mov_b32_e32 v53, v99
	v_mov_b32_e32 v55, v99
	v_mov_b64_e32 v[2:3], s[4:5]
	v_mad_i64_i32 v[2:3], s[4:5], v42, s3, v[2:3]
	v_lshl_add_u64 v[4:5], v[2:3], 0, v[98:99]
	global_load_dwordx4 v[64:67], v[4:5], off sc1
	global_load_dwordx4 v[38:41], v[4:5], off offset:1024 sc1
	global_load_dwordx4 v[34:37], v[4:5], off offset:2048 sc1
	global_load_dwordx4 v[30:33], v[4:5], off offset:3072 sc1
	v_lshl_add_u64 v[4:5], v[2:3], 0, v[52:53]
	global_load_dwordx4 v[26:29], v[4:5], off sc1
	s_mov_b32 s3, 0x42fe0000
	v_lshl_add_u64 v[4:5], v[2:3], 0, v[54:55]
	v_mov_b32_e32 v57, v99
	global_load_dwordx4 v[22:25], v[4:5], off sc1
	v_lshl_add_u64 v[4:5], v[2:3], 0, v[56:57]
	v_mov_b32_e32 v59, v99
	global_load_dwordx4 v[18:21], v[4:5], off sc1
	v_lshl_add_u64 v[4:5], v[2:3], 0, v[58:59]
	v_lshlrev_b32_e32 v98, 1, v46
	global_load_dwordx4 v[14:17], v[4:5], off sc1
	v_lshl_add_u64 v[4:5], v[2:3], 0, v[98:99]
	v_lshlrev_b32_e32 v98, 1, v48
	global_load_dwordx4 v[10:13], v[4:5], off sc1
	v_lshl_add_u64 v[4:5], v[2:3], 0, v[98:99]
	v_lshlrev_b32_e32 v98, 1, v50
	v_lshl_add_u64 v[2:3], v[2:3], 0, v[98:99]
	global_load_dwordx4 v[6:9], v[4:5], off sc1
	s_waitcnt vmcnt(10)
	v_max_f32_e32 v1, v1, v1
	v_max_f32_e32 v1, 0x1e3ce508, v1
	v_div_scale_f32 v43, s[4:5], v1, v1, s3
	v_rcp_f32_e32 v53, v43
	v_readlane_b32 s4, v252, 63
	v_readlane_b32 s5, v253, 0
	global_load_dwordx4 v[2:5], v[2:3], off sc1
	v_fma_f32 v55, -v43, v53, 1.0
	v_fmac_f32_e32 v53, v55, v53
	v_div_scale_f32 v55, vcc, s3, v1, s3
	v_mul_f32_e32 v57, v55, v53
	v_fma_f32 v59, -v43, v57, v55
	v_fmac_f32_e32 v57, v59, v53
	v_fma_f32 v43, -v43, v57, v55
	v_div_fmas_f32 v43, v43, v53, v57
	v_div_fixup_f32 v43, v43, v1, s3
	s_waitcnt vmcnt(10)
	v_and_b32_e32 v55, 0xffff0000, v64
	v_lshlrev_b32_e32 v53, 16, v64
	v_lshlrev_b32_e32 v57, 16, v65
	v_and_b32_e32 v59, 0xffff0000, v65
	v_mul_f32_e32 v55, v43, v55
	v_lshlrev_b32_e32 v64, 16, v66
	v_and_b32_e32 v65, 0xffff0000, v66
	v_lshlrev_b32_e32 v66, 16, v67
	v_mul_f32_e32 v53, v43, v53
	v_rndne_f32_e32 v55, v55
	v_mul_f32_e32 v57, v43, v57
	v_mul_f32_e32 v59, v43, v59
	v_rndne_f32_e32 v53, v53
	v_cvt_i32_f32_e32 v55, v55
	v_rndne_f32_e32 v57, v57
	v_mul_f32_e32 v66, v43, v66
	v_rndne_f32_e32 v59, v59
	v_cvt_i32_f32_e32 v53, v53
	v_cvt_i32_f32_sdwa v57, v57 dst_sel:WORD_1 dst_unused:UNUSED_PAD src0_sel:DWORD
	v_rndne_f32_e32 v66, v66
	v_cvt_i32_f32_e32 v59, v59
	v_cvt_i32_f32_sdwa v66, v66 dst_sel:WORD_1 dst_unused:UNUSED_PAD src0_sel:DWORD
	v_lshlrev_b32_e32 v55, 8, v55
	v_and_b32_e32 v67, 0xffff0000, v67
	v_and_b32_e32 v55, 0xff00, v55
	v_mul_f32_e32 v65, v43, v65
	v_and_b32_e32 v57, 0xff0000, v57
	v_perm_b32 v53, v59, v53, s7
	v_mul_f32_e32 v64, v43, v64
	v_rndne_f32_e32 v65, v65
	v_and_b32_e32 v68, 0xff0000, v66
	v_or3_b32 v66, v53, v55, v57
	v_mul_f32_e32 v53, v43, v67
	v_rndne_f32_e32 v64, v64
	v_cvt_i32_f32_e32 v65, v65
	v_rndne_f32_e32 v53, v53
	v_cvt_i32_f32_e32 v64, v64
	v_cvt_i32_f32_e32 v53, v53
	v_lshlrev_b32_e32 v65, 8, v65
	v_and_b32_e32 v65, 0xff00, v65
	s_waitcnt vmcnt(9)
	v_lshlrev_b32_e32 v55, 16, v39
	v_perm_b32 v53, v53, v64, s7
	v_or3_b32 v67, v53, v65, v68
	v_lshlrev_b32_e32 v53, 16, v38
	v_and_b32_e32 v38, 0xffff0000, v38
	v_and_b32_e32 v39, 0xffff0000, v39
	v_mul_f32_e32 v38, v43, v38
	v_mul_f32_e32 v53, v43, v53
	v_rndne_f32_e32 v38, v38
	v_mul_f32_e32 v55, v43, v55
	v_mul_f32_e32 v39, v43, v39
	v_rndne_f32_e32 v53, v53
	v_cvt_i32_f32_e32 v38, v38
	v_rndne_f32_e32 v55, v55
	v_rndne_f32_e32 v39, v39
	v_cvt_i32_f32_e32 v53, v53
	v_cvt_i32_f32_sdwa v55, v55 dst_sel:WORD_1 dst_unused:UNUSED_PAD src0_sel:DWORD
	v_cvt_i32_f32_e32 v39, v39
	v_lshlrev_b32_e32 v57, 16, v40
	v_and_b32_e32 v40, 0xffff0000, v40
	v_lshlrev_b32_e32 v38, 8, v38
	v_lshlrev_b32_e32 v59, 16, v41
	v_and_b32_e32 v41, 0xffff0000, v41
	v_and_b32_e32 v38, 0xff00, v38
	v_mul_f32_e32 v40, v43, v40
	v_and_b32_e32 v55, 0xff0000, v55
	v_perm_b32 v39, v39, v53, s7
	v_mul_f32_e32 v57, v43, v57
	v_rndne_f32_e32 v40, v40
	v_mul_f32_e32 v59, v43, v59
	v_or3_b32 v38, v39, v38, v55
	v_mul_f32_e32 v39, v43, v41
	v_rndne_f32_e32 v57, v57
	v_cvt_i32_f32_e32 v40, v40
	v_rndne_f32_e32 v59, v59
	v_rndne_f32_e32 v39, v39
	v_cvt_i32_f32_e32 v57, v57
	v_cvt_i32_f32_sdwa v59, v59 dst_sel:WORD_1 dst_unused:UNUSED_PAD src0_sel:DWORD
	v_cvt_i32_f32_e32 v39, v39
	v_mov_b64_e32 v[62:63], s[4:5]
	s_movk_i32 s3, 0x1600
	v_lshlrev_b32_e32 v40, 8, v40
	v_mad_i64_i32 v[62:63], s[4:5], v42, s3, v[62:63]
	v_and_b32_e32 v40, 0xff00, v40
	v_and_b32_e32 v59, 0xff0000, v59
	v_perm_b32 v39, v39, v57, s7
	v_lshl_add_u64 v[64:65], v[62:63], 0, v[44:45]
	v_or3_b32 v39, v39, v40, v59
	global_store_dwordx2 v[64:65], v[38:39], off offset:512
	s_waitcnt vmcnt(9)
	v_lshlrev_b32_e32 v38, 16, v34
	v_and_b32_e32 v34, 0xffff0000, v34
	v_lshlrev_b32_e32 v39, 16, v35
	v_and_b32_e32 v35, 0xffff0000, v35
	v_mul_f32_e32 v34, v43, v34
	v_mul_f32_e32 v38, v43, v38
	v_rndne_f32_e32 v34, v34
	v_mul_f32_e32 v39, v43, v39
	v_mul_f32_e32 v35, v43, v35
	v_rndne_f32_e32 v38, v38
	v_cvt_i32_f32_e32 v34, v34
	v_rndne_f32_e32 v39, v39
	v_rndne_f32_e32 v35, v35
	v_cvt_i32_f32_e32 v38, v38
	v_cvt_i32_f32_sdwa v39, v39 dst_sel:WORD_1 dst_unused:UNUSED_PAD src0_sel:DWORD
	v_cvt_i32_f32_e32 v35, v35
	v_lshlrev_b32_e32 v40, 16, v36
	v_and_b32_e32 v36, 0xffff0000, v36
	v_lshlrev_b32_e32 v34, 8, v34
	v_lshlrev_b32_e32 v41, 16, v37
	v_and_b32_e32 v37, 0xffff0000, v37
	v_and_b32_e32 v34, 0xff00, v34
	v_mul_f32_e32 v36, v43, v36
	v_and_b32_e32 v39, 0xff0000, v39
	v_perm_b32 v35, v35, v38, s7
	v_mul_f32_e32 v40, v43, v40
	v_rndne_f32_e32 v36, v36
	v_mul_f32_e32 v41, v43, v41
	v_or3_b32 v34, v35, v34, v39
	v_mul_f32_e32 v35, v43, v37
	v_rndne_f32_e32 v40, v40
	v_cvt_i32_f32_e32 v36, v36
	v_rndne_f32_e32 v41, v41
	v_rndne_f32_e32 v35, v35
	v_cvt_i32_f32_e32 v40, v40
	v_cvt_i32_f32_sdwa v41, v41 dst_sel:WORD_1 dst_unused:UNUSED_PAD src0_sel:DWORD
	v_cvt_i32_f32_e32 v35, v35
	v_lshlrev_b32_e32 v36, 8, v36
	v_and_b32_e32 v36, 0xff00, v36
	v_and_b32_e32 v41, 0xff0000, v41
	v_perm_b32 v35, v35, v40, s7
	v_or3_b32 v35, v35, v36, v41
	global_store_dwordx2 v[64:65], v[34:35], off offset:1024
	s_waitcnt vmcnt(9)
	v_lshlrev_b32_e32 v34, 16, v30
	v_and_b32_e32 v30, 0xffff0000, v30
	v_lshlrev_b32_e32 v35, 16, v31
	v_and_b32_e32 v31, 0xffff0000, v31
	v_mul_f32_e32 v30, v43, v30
	v_mul_f32_e32 v34, v43, v34
	v_rndne_f32_e32 v30, v30
	v_mul_f32_e32 v35, v43, v35
	v_mul_f32_e32 v31, v43, v31
	v_rndne_f32_e32 v34, v34
	v_cvt_i32_f32_e32 v30, v30
	v_rndne_f32_e32 v35, v35
	v_rndne_f32_e32 v31, v31
	v_cvt_i32_f32_e32 v34, v34
	v_cvt_i32_f32_sdwa v35, v35 dst_sel:WORD_1 dst_unused:UNUSED_PAD src0_sel:DWORD
	v_cvt_i32_f32_e32 v31, v31
	v_lshlrev_b32_e32 v36, 16, v32
	v_and_b32_e32 v32, 0xffff0000, v32
	v_lshlrev_b32_e32 v30, 8, v30
	v_lshlrev_b32_e32 v37, 16, v33
	v_and_b32_e32 v33, 0xffff0000, v33
	v_and_b32_e32 v30, 0xff00, v30
	v_mul_f32_e32 v32, v43, v32
	v_and_b32_e32 v35, 0xff0000, v35
	v_perm_b32 v31, v31, v34, s7
	v_mul_f32_e32 v36, v43, v36
	v_rndne_f32_e32 v32, v32
	v_mul_f32_e32 v37, v43, v37
	v_or3_b32 v30, v31, v30, v35
	v_mul_f32_e32 v31, v43, v33
	v_rndne_f32_e32 v36, v36
	v_cvt_i32_f32_e32 v32, v32
	v_rndne_f32_e32 v37, v37
	v_rndne_f32_e32 v31, v31
	v_cvt_i32_f32_e32 v36, v36
	v_cvt_i32_f32_sdwa v37, v37 dst_sel:WORD_1 dst_unused:UNUSED_PAD src0_sel:DWORD
	v_cvt_i32_f32_e32 v31, v31
	v_lshlrev_b32_e32 v32, 8, v32
	v_and_b32_e32 v32, 0xff00, v32
	v_and_b32_e32 v37, 0xff0000, v37
	v_perm_b32 v31, v31, v36, s7
	v_or3_b32 v31, v31, v32, v37
	global_store_dwordx2 v[64:65], v[30:31], off offset:1536
	s_waitcnt vmcnt(9)
	v_lshlrev_b32_e32 v30, 16, v26
	v_and_b32_e32 v26, 0xffff0000, v26
	v_lshlrev_b32_e32 v31, 16, v27
	v_and_b32_e32 v27, 0xffff0000, v27
	v_mul_f32_e32 v26, v43, v26
	v_mul_f32_e32 v30, v43, v30
	v_rndne_f32_e32 v26, v26
	v_mul_f32_e32 v31, v43, v31
	v_mul_f32_e32 v27, v43, v27
	v_rndne_f32_e32 v30, v30
	v_cvt_i32_f32_e32 v26, v26
	v_rndne_f32_e32 v31, v31
	v_rndne_f32_e32 v27, v27
	v_cvt_i32_f32_e32 v30, v30
	v_cvt_i32_f32_sdwa v31, v31 dst_sel:WORD_1 dst_unused:UNUSED_PAD src0_sel:DWORD
	v_cvt_i32_f32_e32 v27, v27
	v_lshlrev_b32_e32 v32, 16, v28
	v_and_b32_e32 v28, 0xffff0000, v28
	v_lshlrev_b32_e32 v26, 8, v26
	v_lshlrev_b32_e32 v33, 16, v29
	v_and_b32_e32 v29, 0xffff0000, v29
	v_and_b32_e32 v26, 0xff00, v26
	v_mul_f32_e32 v28, v43, v28
	v_and_b32_e32 v31, 0xff0000, v31
	v_perm_b32 v27, v27, v30, s7
	v_mul_f32_e32 v32, v43, v32
	v_rndne_f32_e32 v28, v28
	v_mul_f32_e32 v33, v43, v33
	v_or3_b32 v26, v27, v26, v31
	v_mul_f32_e32 v27, v43, v29
	v_rndne_f32_e32 v32, v32
	v_cvt_i32_f32_e32 v28, v28
	v_rndne_f32_e32 v33, v33
	v_rndne_f32_e32 v27, v27
	v_cvt_i32_f32_e32 v32, v32
	v_cvt_i32_f32_sdwa v33, v33 dst_sel:WORD_1 dst_unused:UNUSED_PAD src0_sel:DWORD
	v_cvt_i32_f32_e32 v27, v27
	v_lshlrev_b32_e32 v28, 8, v28
	v_and_b32_e32 v28, 0xff00, v28
	v_and_b32_e32 v33, 0xff0000, v33
	v_perm_b32 v27, v27, v32, s7
	v_or3_b32 v27, v27, v28, v33
	global_store_dwordx2 v[64:65], v[26:27], off offset:2048
	s_waitcnt vmcnt(9)
	v_lshlrev_b32_e32 v26, 16, v22
	v_and_b32_e32 v22, 0xffff0000, v22
	v_lshlrev_b32_e32 v27, 16, v23
	v_and_b32_e32 v23, 0xffff0000, v23
	v_mul_f32_e32 v22, v43, v22
	v_mul_f32_e32 v26, v43, v26
	v_rndne_f32_e32 v22, v22
	v_mul_f32_e32 v27, v43, v27
	v_mul_f32_e32 v23, v43, v23
	v_rndne_f32_e32 v26, v26
	v_cvt_i32_f32_e32 v22, v22
	v_rndne_f32_e32 v27, v27
	v_rndne_f32_e32 v23, v23
	v_cvt_i32_f32_e32 v26, v26
	v_cvt_i32_f32_sdwa v27, v27 dst_sel:WORD_1 dst_unused:UNUSED_PAD src0_sel:DWORD
	v_cvt_i32_f32_e32 v23, v23
	v_lshlrev_b32_e32 v28, 16, v24
	v_and_b32_e32 v24, 0xffff0000, v24
	v_lshlrev_b32_e32 v22, 8, v22
	v_lshlrev_b32_e32 v29, 16, v25
	v_and_b32_e32 v25, 0xffff0000, v25
	v_and_b32_e32 v22, 0xff00, v22
	v_mul_f32_e32 v24, v43, v24
	v_and_b32_e32 v27, 0xff0000, v27
	v_perm_b32 v23, v23, v26, s7
	v_mul_f32_e32 v28, v43, v28
	v_rndne_f32_e32 v24, v24
	v_mul_f32_e32 v29, v43, v29
	v_or3_b32 v22, v23, v22, v27
	v_mul_f32_e32 v23, v43, v25
	v_rndne_f32_e32 v28, v28
	v_cvt_i32_f32_e32 v24, v24
	v_rndne_f32_e32 v29, v29
	v_rndne_f32_e32 v23, v23
	v_cvt_i32_f32_e32 v28, v28
	v_cvt_i32_f32_sdwa v29, v29 dst_sel:WORD_1 dst_unused:UNUSED_PAD src0_sel:DWORD
	v_cvt_i32_f32_e32 v23, v23
	v_lshlrev_b32_e32 v24, 8, v24
	v_and_b32_e32 v24, 0xff00, v24
	v_and_b32_e32 v29, 0xff0000, v29
	v_perm_b32 v23, v23, v28, s7
	v_or3_b32 v23, v23, v24, v29
	global_store_dwordx2 v[64:65], v[22:23], off offset:2560
	s_waitcnt vmcnt(9)
	v_lshlrev_b32_e32 v22, 16, v18
	v_and_b32_e32 v18, 0xffff0000, v18
	v_lshlrev_b32_e32 v23, 16, v19
	v_and_b32_e32 v19, 0xffff0000, v19
	v_mul_f32_e32 v18, v43, v18
	v_mul_f32_e32 v22, v43, v22
	v_rndne_f32_e32 v18, v18
	v_mul_f32_e32 v23, v43, v23
	v_mul_f32_e32 v19, v43, v19
	v_rndne_f32_e32 v22, v22
	v_cvt_i32_f32_e32 v18, v18
	v_rndne_f32_e32 v23, v23
	v_rndne_f32_e32 v19, v19
	v_cvt_i32_f32_e32 v22, v22
	v_cvt_i32_f32_sdwa v23, v23 dst_sel:WORD_1 dst_unused:UNUSED_PAD src0_sel:DWORD
	v_cvt_i32_f32_e32 v19, v19
	v_lshlrev_b32_e32 v24, 16, v20
	v_and_b32_e32 v20, 0xffff0000, v20
	v_lshlrev_b32_e32 v18, 8, v18
	v_lshlrev_b32_e32 v25, 16, v21
	v_and_b32_e32 v21, 0xffff0000, v21
	v_and_b32_e32 v18, 0xff00, v18
	v_mul_f32_e32 v20, v43, v20
	v_and_b32_e32 v23, 0xff0000, v23
	v_perm_b32 v19, v19, v22, s7
	v_mul_f32_e32 v24, v43, v24
	v_rndne_f32_e32 v20, v20
	v_mul_f32_e32 v25, v43, v25
	v_or3_b32 v18, v19, v18, v23
	v_mul_f32_e32 v19, v43, v21
	v_rndne_f32_e32 v24, v24
	v_cvt_i32_f32_e32 v20, v20
	v_rndne_f32_e32 v25, v25
	v_rndne_f32_e32 v19, v19
	v_cvt_i32_f32_e32 v24, v24
	v_cvt_i32_f32_sdwa v25, v25 dst_sel:WORD_1 dst_unused:UNUSED_PAD src0_sel:DWORD
	v_cvt_i32_f32_e32 v19, v19
	v_lshlrev_b32_e32 v20, 8, v20
	v_and_b32_e32 v20, 0xff00, v20
	v_and_b32_e32 v25, 0xff0000, v25
	v_perm_b32 v19, v19, v24, s7
	v_or3_b32 v19, v19, v20, v25
	global_store_dwordx2 v[64:65], v[18:19], off offset:3072
	s_waitcnt vmcnt(9)
	v_lshlrev_b32_e32 v18, 16, v14
	v_and_b32_e32 v14, 0xffff0000, v14
	v_lshlrev_b32_e32 v19, 16, v15
	v_and_b32_e32 v15, 0xffff0000, v15
	v_mul_f32_e32 v14, v43, v14
	v_mul_f32_e32 v18, v43, v18
	v_rndne_f32_e32 v14, v14
	v_mul_f32_e32 v19, v43, v19
	v_mul_f32_e32 v15, v43, v15
	v_rndne_f32_e32 v18, v18
	v_cvt_i32_f32_e32 v14, v14
	v_rndne_f32_e32 v19, v19
	v_rndne_f32_e32 v15, v15
	v_cvt_i32_f32_e32 v18, v18
	v_cvt_i32_f32_sdwa v19, v19 dst_sel:WORD_1 dst_unused:UNUSED_PAD src0_sel:DWORD
	v_cvt_i32_f32_e32 v15, v15
	v_lshlrev_b32_e32 v20, 16, v16
	v_and_b32_e32 v16, 0xffff0000, v16
	v_lshlrev_b32_e32 v14, 8, v14
	v_lshlrev_b32_e32 v21, 16, v17
	v_and_b32_e32 v17, 0xffff0000, v17
	v_and_b32_e32 v14, 0xff00, v14
	v_mul_f32_e32 v16, v43, v16
	v_and_b32_e32 v19, 0xff0000, v19
	v_perm_b32 v15, v15, v18, s7
	v_mul_f32_e32 v20, v43, v20
	v_rndne_f32_e32 v16, v16
	v_mul_f32_e32 v21, v43, v21
	v_or3_b32 v14, v15, v14, v19
	v_mul_f32_e32 v15, v43, v17
	v_rndne_f32_e32 v20, v20
	v_cvt_i32_f32_e32 v16, v16
	v_rndne_f32_e32 v21, v21
	v_rndne_f32_e32 v15, v15
	v_cvt_i32_f32_e32 v20, v20
	v_cvt_i32_f32_sdwa v21, v21 dst_sel:WORD_1 dst_unused:UNUSED_PAD src0_sel:DWORD
	v_cvt_i32_f32_e32 v15, v15
	v_lshlrev_b32_e32 v16, 8, v16
	v_and_b32_e32 v16, 0xff00, v16
	v_and_b32_e32 v21, 0xff0000, v21
	v_perm_b32 v15, v15, v20, s7
	v_or3_b32 v15, v15, v16, v21
	global_store_dwordx2 v[64:65], v[14:15], off offset:3584
	s_waitcnt vmcnt(9)
	v_lshlrev_b32_e32 v14, 16, v10
	v_and_b32_e32 v10, 0xffff0000, v10
	v_lshlrev_b32_e32 v15, 16, v11
	v_and_b32_e32 v11, 0xffff0000, v11
	v_mul_f32_e32 v10, v43, v10
	v_mul_f32_e32 v14, v43, v14
	v_rndne_f32_e32 v10, v10
	v_mul_f32_e32 v15, v43, v15
	v_mul_f32_e32 v11, v43, v11
	v_rndne_f32_e32 v14, v14
	v_cvt_i32_f32_e32 v10, v10
	v_rndne_f32_e32 v15, v15
	v_rndne_f32_e32 v11, v11
	v_cvt_i32_f32_e32 v14, v14
	v_cvt_i32_f32_sdwa v15, v15 dst_sel:WORD_1 dst_unused:UNUSED_PAD src0_sel:DWORD
	v_cvt_i32_f32_e32 v11, v11
	v_lshlrev_b32_e32 v16, 16, v12
	v_and_b32_e32 v12, 0xffff0000, v12
	v_lshlrev_b32_e32 v10, 8, v10
	v_lshlrev_b32_e32 v17, 16, v13
	v_and_b32_e32 v13, 0xffff0000, v13
	v_and_b32_e32 v10, 0xff00, v10
	v_mul_f32_e32 v12, v43, v12
	v_and_b32_e32 v15, 0xff0000, v15
	v_perm_b32 v11, v11, v14, s7
	v_mul_f32_e32 v16, v43, v16
	v_rndne_f32_e32 v12, v12
	v_mul_f32_e32 v17, v43, v17
	v_or3_b32 v10, v11, v10, v15
	v_mul_f32_e32 v11, v43, v13
	v_rndne_f32_e32 v16, v16
	v_cvt_i32_f32_e32 v12, v12
	v_rndne_f32_e32 v17, v17
	v_rndne_f32_e32 v11, v11
	v_cvt_i32_f32_e32 v16, v16
	v_cvt_i32_f32_sdwa v17, v17 dst_sel:WORD_1 dst_unused:UNUSED_PAD src0_sel:DWORD
	v_cvt_i32_f32_e32 v11, v11
	v_lshlrev_b32_e32 v12, 8, v12
	v_and_b32_e32 v12, 0xff00, v12
	v_and_b32_e32 v17, 0xff0000, v17
	v_perm_b32 v11, v11, v16, s7
	v_or3_b32 v11, v11, v12, v17
	v_lshl_add_u64 v[12:13], v[62:63], 0, v[46:47]
	global_store_dwordx2 v[12:13], v[10:11], off
	s_waitcnt vmcnt(9)
	v_lshlrev_b32_e32 v10, 16, v6
	v_and_b32_e32 v6, 0xffff0000, v6
	v_lshlrev_b32_e32 v11, 16, v7
	v_and_b32_e32 v7, 0xffff0000, v7
	v_mul_f32_e32 v6, v43, v6
	v_mul_f32_e32 v10, v43, v10
	v_rndne_f32_e32 v6, v6
	v_mul_f32_e32 v11, v43, v11
	v_mul_f32_e32 v7, v43, v7
	v_rndne_f32_e32 v10, v10
	v_cvt_i32_f32_e32 v6, v6
	v_rndne_f32_e32 v11, v11
	v_rndne_f32_e32 v7, v7
	v_cvt_i32_f32_e32 v10, v10
	v_cvt_i32_f32_sdwa v11, v11 dst_sel:WORD_1 dst_unused:UNUSED_PAD src0_sel:DWORD
	v_cvt_i32_f32_e32 v7, v7
	v_lshlrev_b32_e32 v12, 16, v8
	v_and_b32_e32 v8, 0xffff0000, v8
	v_lshlrev_b32_e32 v6, 8, v6
	v_lshlrev_b32_e32 v13, 16, v9
	v_and_b32_e32 v9, 0xffff0000, v9
	v_and_b32_e32 v6, 0xff00, v6
	v_mul_f32_e32 v8, v43, v8
	v_and_b32_e32 v11, 0xff0000, v11
	v_perm_b32 v7, v7, v10, s7
	v_mul_f32_e32 v12, v43, v12
	v_rndne_f32_e32 v8, v8
	v_mul_f32_e32 v13, v43, v13
	v_or3_b32 v6, v7, v6, v11
	v_mul_f32_e32 v7, v43, v9
	v_rndne_f32_e32 v12, v12
	v_cvt_i32_f32_e32 v8, v8
	v_rndne_f32_e32 v13, v13
	v_rndne_f32_e32 v7, v7
	v_cvt_i32_f32_e32 v12, v12
	v_cvt_i32_f32_sdwa v13, v13 dst_sel:WORD_1 dst_unused:UNUSED_PAD src0_sel:DWORD
	v_cvt_i32_f32_e32 v7, v7
	v_lshlrev_b32_e32 v8, 8, v8
	v_and_b32_e32 v8, 0xff00, v8
	v_and_b32_e32 v13, 0xff0000, v13
	v_perm_b32 v7, v7, v12, s7
	v_or3_b32 v7, v7, v8, v13
	v_lshl_add_u64 v[8:9], v[62:63], 0, v[48:49]
	global_store_dwordx2 v[8:9], v[6:7], off
	s_waitcnt vmcnt(9)
	v_lshlrev_b32_e32 v6, 16, v2
	v_and_b32_e32 v2, 0xffff0000, v2
	v_lshlrev_b32_e32 v7, 16, v3
	v_and_b32_e32 v3, 0xffff0000, v3
	v_mul_f32_e32 v2, v43, v2
	v_mul_f32_e32 v6, v43, v6
	v_rndne_f32_e32 v2, v2
	v_mul_f32_e32 v7, v43, v7
	v_mul_f32_e32 v3, v43, v3
	v_rndne_f32_e32 v6, v6
	v_cvt_i32_f32_e32 v2, v2
	v_rndne_f32_e32 v7, v7
	v_rndne_f32_e32 v3, v3
	v_cvt_i32_f32_e32 v6, v6
	v_cvt_i32_f32_sdwa v7, v7 dst_sel:WORD_1 dst_unused:UNUSED_PAD src0_sel:DWORD
	v_cvt_i32_f32_e32 v3, v3
	v_lshlrev_b32_e32 v8, 16, v4
	v_and_b32_e32 v4, 0xffff0000, v4
	v_lshlrev_b32_e32 v2, 8, v2
	v_lshlrev_b32_e32 v9, 16, v5
	v_and_b32_e32 v5, 0xffff0000, v5
	v_and_b32_e32 v2, 0xff00, v2
	v_mul_f32_e32 v4, v43, v4
	v_and_b32_e32 v7, 0xff0000, v7
	v_perm_b32 v3, v3, v6, s7
	v_mul_f32_e32 v8, v43, v8
	v_rndne_f32_e32 v4, v4
	v_mul_f32_e32 v9, v43, v9
	v_or3_b32 v2, v3, v2, v7
	v_mul_f32_e32 v3, v43, v5
	v_rndne_f32_e32 v8, v8
	v_cvt_i32_f32_e32 v4, v4
	v_rndne_f32_e32 v9, v9
	v_rndne_f32_e32 v3, v3
	v_cvt_i32_f32_e32 v8, v8
	v_cvt_i32_f32_sdwa v9, v9 dst_sel:WORD_1 dst_unused:UNUSED_PAD src0_sel:DWORD
	v_cvt_i32_f32_e32 v3, v3
	v_lshlrev_b32_e32 v4, 8, v4
	v_and_b32_e32 v4, 0xff00, v4
	v_and_b32_e32 v9, 0xff0000, v9
	v_perm_b32 v3, v3, v8, s7
	v_or3_b32 v3, v3, v4, v9
	v_lshl_add_u64 v[4:5], v[62:63], 0, v[50:51]
	global_store_dwordx2 v[64:65], v[66:67], off
	global_store_dwordx2 v[4:5], v[2:3], off
	s_and_saveexec_b64 s[4:5], s[0:1]
	s_cbranch_execz .LBB0_2162
	v_mul_f32_e32 v1, 0x3c010204, v1
	global_store_dword v[60:61], v1, off
	s_branch .LBB0_2162

.LBB0_2295:
	s_or_b64 exec, exec, s[4:5]
	s_mov_b64 s[22:23], exec
	v_mbcnt_lo_u32_b32 v1, s22, 0
	v_mbcnt_hi_u32_b32 v1, s23, v1
	v_cmp_eq_u32_e32 vcc, 0, v1
	s_waitcnt vmcnt(0)
	s_and_saveexec_b64 s[24:25], vcc
	s_cbranch_execnz .LBB0_2296
	s_getpc_b64 s[98:99]
